# saddr-form LDS-DMA loads (64-bit VALU address adds removed) also in the merge, w_o and expert-down GEMM loops; on top of v118
# speedup vs baseline: 1.0062x; 1.0014x over previous
.LBB0_1332:
	s_add_u32 s0, s6, 0xfffe0080
	s_addc_u32 s1, s7, -1
	s_add_i32 s33, 0, 0x10000
	s_cmp_eq_u32 s86, 4
	s_cselect_b32 s31, s23, s1
	s_cselect_b32 s30, s22, s0
	s_cselect_b32 s29, s15, s82
	s_cselect_b32 s28, s17, s21
	s_add_i32 m0, s70, 0xc000
	ds_read_b128 v[146:149], v240
	ds_read_b128 v[150:153], v240 offset:1024
	ds_read_b128 v[154:157], v240 offset:2048
	ds_read_b128 v[158:161], v240 offset:3072
	ds_read_b128 v[162:165], v240 offset:4096
	ds_read_b128 v[166:169], v240 offset:5120
	ds_read_b128 v[170:173], v240 offset:6144
	ds_read_b128 v[174:177], v240 offset:7168
	global_load_lds_dwordx4 v214, s[6:7]
	s_add_i32 m0, s70, 0xe000
	s_nop 0
	global_load_lds_dwordx4 v216, s[6:7]
	s_waitcnt lgkmcnt(8)
	s_barrier
	s_waitcnt lgkmcnt(0)
	v_mfma_f32_16x16x32_bf16 v[62:65], v[130:133], v[146:149], v[62:65]
	v_mfma_f32_16x16x32_bf16 v[58:61], v[138:141], v[146:149], v[58:61]
	v_mfma_f32_16x16x32_bf16 v[54:57], v[130:133], v[154:157], v[54:57]
	v_mfma_f32_16x16x32_bf16 v[50:53], v[138:141], v[154:157], v[50:53]
	v_mfma_f32_16x16x32_bf16 v[46:49], v[130:133], v[162:165], v[46:49]
	v_mfma_f32_16x16x32_bf16 v[42:45], v[138:141], v[162:165], v[42:45]
	v_mfma_f32_16x16x32_bf16 v[38:41], v[130:133], v[170:173], v[38:41]
	v_mfma_f32_16x16x32_bf16 v[34:37], v[138:141], v[170:173], v[34:37]
	v_mfma_f32_16x16x32_bf16 v[62:65], v[134:137], v[150:153], v[62:65]
	v_mfma_f32_16x16x32_bf16 v[58:61], v[142:145], v[150:153], v[58:61]
	v_mfma_f32_16x16x32_bf16 v[54:57], v[134:137], v[158:161], v[54:57]
	v_mfma_f32_16x16x32_bf16 v[50:53], v[142:145], v[158:161], v[50:53]
	v_mfma_f32_16x16x32_bf16 v[46:49], v[134:137], v[166:169], v[46:49]
	v_mfma_f32_16x16x32_bf16 v[42:45], v[142:145], v[166:169], v[42:45]
	v_mfma_f32_16x16x32_bf16 v[38:41], v[134:137], v[174:177], v[38:41]
	v_mfma_f32_16x16x32_bf16 v[34:37], v[142:145], v[174:177], v[34:37]
	s_barrier
	s_add_i32 s36, 0, 0x14000
	s_add_i32 s0, s33, s66
	v_add_u32_e32 v190, s36, v237
	v_lshl_add_u64 v[218:219], s[28:29], 0, v[202:203]
	s_mov_b32 m0, s0
	ds_read_b128 v[178:181], v190
	ds_read_b128 v[182:185], v190 offset:1024
	ds_read_b128 v[186:189], v190 offset:2048
	ds_read_b128 v[190:193], v190 offset:3072
	global_load_lds_dwordx4 v[218:219], off
	v_lshl_add_u64 v[220:221], s[28:29], 0, v[198:199]
	s_add_i32 m0, s0, 0x2000
	s_nop 0
	global_load_lds_dwordx4 v[220:221], off
	s_barrier
	s_waitcnt lgkmcnt(0)
	v_mfma_f32_16x16x32_bf16 v[30:33], v[178:181], v[146:149], v[30:33]
	v_mfma_f32_16x16x32_bf16 v[26:29], v[186:189], v[146:149], v[26:29]
	v_mfma_f32_16x16x32_bf16 v[22:25], v[178:181], v[154:157], v[22:25]
	v_mfma_f32_16x16x32_bf16 v[18:21], v[186:189], v[154:157], v[18:21]
	v_mfma_f32_16x16x32_bf16 v[14:17], v[178:181], v[162:165], v[14:17]
	v_mfma_f32_16x16x32_bf16 v[10:13], v[186:189], v[162:165], v[10:13]
	v_mfma_f32_16x16x32_bf16 v[6:9], v[178:181], v[170:173], v[6:9]
	v_mfma_f32_16x16x32_bf16 v[2:5], v[186:189], v[170:173], v[2:5]
	v_mfma_f32_16x16x32_bf16 v[30:33], v[182:185], v[150:153], v[30:33]
	v_mfma_f32_16x16x32_bf16 v[26:29], v[190:193], v[150:153], v[26:29]
	v_mfma_f32_16x16x32_bf16 v[22:25], v[182:185], v[158:161], v[22:25]
	v_mfma_f32_16x16x32_bf16 v[18:21], v[190:193], v[158:161], v[18:21]
	v_mfma_f32_16x16x32_bf16 v[14:17], v[182:185], v[166:169], v[14:17]
	v_mfma_f32_16x16x32_bf16 v[10:13], v[190:193], v[166:169], v[10:13]
	v_mfma_f32_16x16x32_bf16 v[6:9], v[182:185], v[174:177], v[6:9]
	v_mfma_f32_16x16x32_bf16 v[2:5], v[190:193], v[174:177], v[2:5]
	s_mov_b32 m0, s70
	v_lshl_add_u64 v[224:225], s[30:31], 0, v[204:205]
	s_barrier
	ds_read_b128 v[146:149], v240 offset:16384
	ds_read_b128 v[150:153], v240 offset:17408
	ds_read_b128 v[154:157], v240 offset:18432
	ds_read_b128 v[158:161], v240 offset:19456
	ds_read_b128 v[162:165], v240 offset:20480
	ds_read_b128 v[166:169], v240 offset:21504
	ds_read_b128 v[170:173], v240 offset:22528
	ds_read_b128 v[174:177], v240 offset:23552
	global_load_lds_dwordx4 v[224:225], off
	v_lshl_add_u64 v[230:231], s[30:31], 0, v[200:201]
	s_mov_b32 m0, s71
	s_nop 0
	global_load_lds_dwordx4 v[230:231], off
	s_waitcnt vmcnt(10)
	s_barrier
	s_waitcnt lgkmcnt(0)
	v_mfma_f32_16x16x32_bf16 v[66:69], v[130:133], v[146:149], v[66:69]
	v_mfma_f32_16x16x32_bf16 v[70:73], v[138:141], v[146:149], v[70:73]
	v_mfma_f32_16x16x32_bf16 v[74:77], v[130:133], v[154:157], v[74:77]
	v_mfma_f32_16x16x32_bf16 v[78:81], v[138:141], v[154:157], v[78:81]
	v_mfma_f32_16x16x32_bf16 v[82:85], v[130:133], v[162:165], v[82:85]
	v_mfma_f32_16x16x32_bf16 v[86:89], v[138:141], v[162:165], v[86:89]
	v_mfma_f32_16x16x32_bf16 v[90:93], v[130:133], v[170:173], v[90:93]
	v_mfma_f32_16x16x32_bf16 v[94:97], v[138:141], v[170:173], v[94:97]
	v_mfma_f32_16x16x32_bf16 v[66:69], v[134:137], v[150:153], v[66:69]
	v_mfma_f32_16x16x32_bf16 v[70:73], v[142:145], v[150:153], v[70:73]
	v_mfma_f32_16x16x32_bf16 v[74:77], v[134:137], v[158:161], v[74:77]
	v_mfma_f32_16x16x32_bf16 v[78:81], v[142:145], v[158:161], v[78:81]
	v_mfma_f32_16x16x32_bf16 v[82:85], v[134:137], v[166:169], v[82:85]
	v_mfma_f32_16x16x32_bf16 v[86:89], v[142:145], v[166:169], v[86:89]
	v_mfma_f32_16x16x32_bf16 v[90:93], v[134:137], v[174:177], v[90:93]
	v_mfma_f32_16x16x32_bf16 v[94:97], v[142:145], v[174:177], v[94:97]
	s_barrier
	s_add_u32 s0, s28, 0x20000
	s_addc_u32 s1, s29, 0
	s_add_i32 s33, s36, s66
	s_mov_b32 m0, s33
	s_nop 0
	global_load_lds_dwordx4 v202, s[0:1]
	s_add_i32 m0, s33, 0x2000
	s_nop 0
	global_load_lds_dwordx4 v198, s[0:1]
	v_add_u32_e32 v142, 0x18000, v237
	ds_read_b128 v[130:133], v142
	ds_read_b128 v[134:137], v142 offset:1024
	ds_read_b128 v[138:141], v142 offset:2048
	ds_read_b128 v[142:145], v142 offset:3072
	s_waitcnt vmcnt(6)
	s_barrier
	v_mfma_f32_16x16x32_bf16 v[98:101], v[178:181], v[146:149], v[98:101]
	v_mfma_f32_16x16x32_bf16 v[102:105], v[186:189], v[146:149], v[102:105]
	v_mfma_f32_16x16x32_bf16 v[106:109], v[178:181], v[154:157], v[106:109]
	v_mfma_f32_16x16x32_bf16 v[110:113], v[186:189], v[154:157], v[110:113]
	v_mfma_f32_16x16x32_bf16 v[114:117], v[178:181], v[162:165], v[114:117]
	v_mfma_f32_16x16x32_bf16 v[118:121], v[186:189], v[162:165], v[118:121]
	v_mfma_f32_16x16x32_bf16 v[122:125], v[178:181], v[170:173], v[122:125]
	v_mfma_f32_16x16x32_bf16 v[126:129], v[186:189], v[170:173], v[126:129]
	v_mfma_f32_16x16x32_bf16 v[98:101], v[182:185], v[150:153], v[98:101]
	v_mfma_f32_16x16x32_bf16 v[102:105], v[190:193], v[150:153], v[102:105]
	v_mfma_f32_16x16x32_bf16 v[106:109], v[182:185], v[158:161], v[106:109]
	v_mfma_f32_16x16x32_bf16 v[110:113], v[190:193], v[158:161], v[110:113]
	v_mfma_f32_16x16x32_bf16 v[114:117], v[182:185], v[166:169], v[114:117]
	v_mfma_f32_16x16x32_bf16 v[118:121], v[190:193], v[166:169], v[118:121]
	v_mfma_f32_16x16x32_bf16 v[122:125], v[182:185], v[174:177], v[122:125]
	v_mfma_f32_16x16x32_bf16 v[126:129], v[190:193], v[174:177], v[126:129]
	s_add_i32 s33, 0, 0x18000
	s_barrier
	s_add_u32 s0, s30, 0x20000
	s_addc_u32 s1, s31, 0
	s_mov_b32 m0, s72
	ds_read_b128 v[146:149], v240 offset:32768
	ds_read_b128 v[150:153], v240 offset:33792
	ds_read_b128 v[154:157], v240 offset:34816
	ds_read_b128 v[158:161], v240 offset:35840
	ds_read_b128 v[162:165], v240 offset:36864
	ds_read_b128 v[166:169], v240 offset:37888
	ds_read_b128 v[170:173], v240 offset:38912
	ds_read_b128 v[174:177], v240 offset:39936
	global_load_lds_dwordx4 v204, s[0:1]
	s_mov_b32 m0, s73
	s_nop 0
	global_load_lds_dwordx4 v200, s[0:1]
	s_waitcnt lgkmcnt(8)
	s_barrier
	s_waitcnt lgkmcnt(0)
	v_mfma_f32_16x16x32_bf16 v[62:65], v[130:133], v[146:149], v[62:65]
	v_mfma_f32_16x16x32_bf16 v[58:61], v[138:141], v[146:149], v[58:61]
	v_mfma_f32_16x16x32_bf16 v[54:57], v[130:133], v[154:157], v[54:57]
	v_mfma_f32_16x16x32_bf16 v[50:53], v[138:141], v[154:157], v[50:53]
	v_mfma_f32_16x16x32_bf16 v[46:49], v[130:133], v[162:165], v[46:49]
	v_mfma_f32_16x16x32_bf16 v[42:45], v[138:141], v[162:165], v[42:45]
	v_mfma_f32_16x16x32_bf16 v[38:41], v[130:133], v[170:173], v[38:41]
	v_mfma_f32_16x16x32_bf16 v[34:37], v[138:141], v[170:173], v[34:37]
	v_mfma_f32_16x16x32_bf16 v[62:65], v[134:137], v[150:153], v[62:65]
	v_mfma_f32_16x16x32_bf16 v[58:61], v[142:145], v[150:153], v[58:61]
	v_mfma_f32_16x16x32_bf16 v[54:57], v[134:137], v[158:161], v[54:57]
	v_mfma_f32_16x16x32_bf16 v[50:53], v[142:145], v[158:161], v[50:53]
	v_mfma_f32_16x16x32_bf16 v[46:49], v[134:137], v[166:169], v[46:49]
	v_mfma_f32_16x16x32_bf16 v[42:45], v[142:145], v[166:169], v[42:45]
	v_mfma_f32_16x16x32_bf16 v[38:41], v[134:137], v[174:177], v[38:41]
	v_mfma_f32_16x16x32_bf16 v[34:37], v[142:145], v[174:177], v[34:37]
	s_barrier
	s_add_i32 s30, 0, 0x1c000
	s_add_i32 s0, s33, s66
	v_add_u32_e32 v190, s30, v237
	v_lshl_add_u64 v[218:219], v[218:219], 0, s[54:55]
	s_mov_b32 m0, s0
	ds_read_b128 v[178:181], v190
	ds_read_b128 v[182:185], v190 offset:1024
	ds_read_b128 v[186:189], v190 offset:2048
	ds_read_b128 v[190:193], v190 offset:3072
	global_load_lds_dwordx4 v[218:219], off
	v_lshl_add_u64 v[218:219], v[220:221], 0, s[54:55]
	s_add_i32 m0, s0, 0x2000
	s_nop 0
	global_load_lds_dwordx4 v[218:219], off
	s_barrier
	s_waitcnt lgkmcnt(0)
	v_mfma_f32_16x16x32_bf16 v[30:33], v[178:181], v[146:149], v[30:33]
	v_mfma_f32_16x16x32_bf16 v[26:29], v[186:189], v[146:149], v[26:29]
	v_mfma_f32_16x16x32_bf16 v[22:25], v[178:181], v[154:157], v[22:25]
	v_mfma_f32_16x16x32_bf16 v[18:21], v[186:189], v[154:157], v[18:21]
	v_mfma_f32_16x16x32_bf16 v[14:17], v[178:181], v[162:165], v[14:17]
	v_mfma_f32_16x16x32_bf16 v[10:13], v[186:189], v[162:165], v[10:13]
	v_mfma_f32_16x16x32_bf16 v[6:9], v[178:181], v[170:173], v[6:9]
	v_mfma_f32_16x16x32_bf16 v[2:5], v[186:189], v[170:173], v[2:5]
	v_mfma_f32_16x16x32_bf16 v[30:33], v[182:185], v[150:153], v[30:33]
	v_mfma_f32_16x16x32_bf16 v[26:29], v[190:193], v[150:153], v[26:29]
	v_mfma_f32_16x16x32_bf16 v[22:25], v[182:185], v[158:161], v[22:25]
	v_mfma_f32_16x16x32_bf16 v[18:21], v[190:193], v[158:161], v[18:21]
	v_mfma_f32_16x16x32_bf16 v[14:17], v[182:185], v[166:169], v[14:17]
	v_mfma_f32_16x16x32_bf16 v[10:13], v[190:193], v[166:169], v[10:13]
	v_mfma_f32_16x16x32_bf16 v[6:9], v[182:185], v[174:177], v[6:9]
	v_mfma_f32_16x16x32_bf16 v[2:5], v[190:193], v[174:177], v[2:5]
	s_mov_b32 m0, s76
	v_lshl_add_u64 v[218:219], v[224:225], 0, s[54:55]
	s_barrier
	ds_read_b128 v[146:149], v240 offset:49152
	ds_read_b128 v[150:153], v240 offset:50176
	ds_read_b128 v[154:157], v240 offset:51200
	ds_read_b128 v[158:161], v240 offset:52224
	ds_read_b128 v[162:165], v240 offset:53248
	ds_read_b128 v[166:169], v240 offset:54272
	ds_read_b128 v[170:173], v240 offset:55296
	ds_read_b128 v[174:177], v240 offset:56320
	global_load_lds_dwordx4 v[218:219], off
	v_lshl_add_u64 v[218:219], v[230:231], 0, s[54:55]
	s_mov_b32 m0, s77
	s_nop 0
	global_load_lds_dwordx4 v[218:219], off
	s_waitcnt vmcnt(10)
	s_barrier
	s_waitcnt lgkmcnt(0)
	v_mfma_f32_16x16x32_bf16 v[66:69], v[130:133], v[146:149], v[66:69]
	v_mfma_f32_16x16x32_bf16 v[70:73], v[138:141], v[146:149], v[70:73]
	v_mfma_f32_16x16x32_bf16 v[74:77], v[130:133], v[154:157], v[74:77]
	v_mfma_f32_16x16x32_bf16 v[78:81], v[138:141], v[154:157], v[78:81]
	v_mfma_f32_16x16x32_bf16 v[82:85], v[130:133], v[162:165], v[82:85]
	v_mfma_f32_16x16x32_bf16 v[86:89], v[138:141], v[162:165], v[86:89]
	v_mfma_f32_16x16x32_bf16 v[90:93], v[130:133], v[170:173], v[90:93]
	v_mfma_f32_16x16x32_bf16 v[94:97], v[138:141], v[170:173], v[94:97]
	v_mfma_f32_16x16x32_bf16 v[66:69], v[134:137], v[150:153], v[66:69]
	v_mfma_f32_16x16x32_bf16 v[70:73], v[142:145], v[150:153], v[70:73]
	v_mfma_f32_16x16x32_bf16 v[74:77], v[134:137], v[158:161], v[74:77]
	v_mfma_f32_16x16x32_bf16 v[78:81], v[142:145], v[158:161], v[78:81]
	v_mfma_f32_16x16x32_bf16 v[82:85], v[134:137], v[166:169], v[82:85]
	v_mfma_f32_16x16x32_bf16 v[86:89], v[142:145], v[166:169], v[86:89]
	v_mfma_f32_16x16x32_bf16 v[90:93], v[134:137], v[174:177], v[90:93]
	v_mfma_f32_16x16x32_bf16 v[94:97], v[142:145], v[174:177], v[94:97]
	s_barrier
	s_add_u32 s0, s28, 0x20080
	s_addc_u32 s1, s29, 0
	s_add_i32 s28, s30, s66
	s_mov_b32 m0, s28
	s_nop 0
	global_load_lds_dwordx4 v202, s[0:1]
	s_add_i32 m0, s28, 0x2000
	s_nop 0
	global_load_lds_dwordx4 v198, s[0:1]
	v_add_u32_e32 v142, 0x10000, v237
	ds_read_b128 v[130:133], v142
	ds_read_b128 v[134:137], v142 offset:1024
	ds_read_b128 v[138:141], v142 offset:2048
	ds_read_b128 v[142:145], v142 offset:3072
	s_waitcnt vmcnt(6)
	s_barrier
	v_mfma_f32_16x16x32_bf16 v[98:101], v[178:181], v[146:149], v[98:101]
	v_mfma_f32_16x16x32_bf16 v[102:105], v[186:189], v[146:149], v[102:105]
	v_mfma_f32_16x16x32_bf16 v[106:109], v[178:181], v[154:157], v[106:109]
	v_mfma_f32_16x16x32_bf16 v[110:113], v[186:189], v[154:157], v[110:113]
	v_mfma_f32_16x16x32_bf16 v[114:117], v[178:181], v[162:165], v[114:117]
	v_mfma_f32_16x16x32_bf16 v[118:121], v[186:189], v[162:165], v[118:121]
	v_mfma_f32_16x16x32_bf16 v[122:125], v[178:181], v[170:173], v[122:125]
	v_mfma_f32_16x16x32_bf16 v[126:129], v[186:189], v[170:173], v[126:129]
	v_mfma_f32_16x16x32_bf16 v[98:101], v[182:185], v[150:153], v[98:101]
	v_mfma_f32_16x16x32_bf16 v[102:105], v[190:193], v[150:153], v[102:105]
	v_mfma_f32_16x16x32_bf16 v[106:109], v[182:185], v[158:161], v[106:109]
	v_mfma_f32_16x16x32_bf16 v[110:113], v[190:193], v[158:161], v[110:113]
	v_mfma_f32_16x16x32_bf16 v[114:117], v[182:185], v[166:169], v[114:117]
	v_mfma_f32_16x16x32_bf16 v[118:121], v[190:193], v[166:169], v[118:121]
	v_mfma_f32_16x16x32_bf16 v[122:125], v[182:185], v[174:177], v[122:125]
	v_mfma_f32_16x16x32_bf16 v[126:129], v[190:193], v[174:177], v[126:129]
	s_add_i32 s86, s86, 2
	s_add_u32 s6, s6, 0x100
	s_addc_u32 s7, s7, 0
	s_add_u32 s21, s21, 0x100
	s_addc_u32 s82, s82, 0
	s_cmp_gt_u32 s86, 5
	s_barrier
	s_cbranch_scc0 .LBB0_1332
	s_waitcnt lgkmcnt(0)
	s_cmp_lg_u32 s27, 0
	s_cselect_b64 s[6:7], -1, 0
	s_cmp_eq_u32 s27, 0
	v_lshl_add_u32 v218, s26, 8, v1
	s_cselect_b32 s0, 0, 0x10000
	s_add_u32 s26, s74, s0
	v_ashrrev_i32_e32 v130, 5, v218
	s_addc_u32 s27, s75, 0
	v_and_b32_e32 v136, -8, v130
	s_lshl_b32 s0, s79, 1
	v_add_u32_e32 v130, s0, v136
	v_ashrrev_i32_e32 v131, 31, v130
	v_lshlrev_b64 v[130:131], 17, v[130:131]
	v_lshl_add_u64 v[132:133], v[206:207], 1, s[26:27]
	v_lshl_add_u64 v[134:135], v[132:133], 0, v[130:131]
	s_or_b32 s1, s0, 1
	global_load_dwordx4 v[186:189], v[134:135], off
	v_add_u32_e32 v134, s1, v136
	v_ashrrev_i32_e32 v135, 31, v134
	v_lshlrev_b64 v[134:135], 17, v[134:135]
	v_lshl_add_u64 v[132:133], v[132:133], 0, v[134:135]
	global_load_dwordx4 v[178:181], v[132:133], off
	v_lshl_add_u64 v[132:133], v[208:209], 1, s[26:27]
	v_lshl_add_u64 v[136:137], v[132:133], 0, v[130:131]
	global_load_dwordx4 v[174:177], v[136:137], off
	v_lshl_add_u64 v[132:133], v[132:133], 0, v[134:135]
	global_load_dwordx4 v[170:173], v[132:133], off
	v_lshl_add_u64 v[132:133], v[210:211], 1, s[26:27]
	v_lshl_add_u64 v[136:137], v[132:133], 0, v[130:131]
	v_lshl_add_u64 v[132:133], v[132:133], 0, v[134:135]
	global_load_dwordx4 v[162:165], v[136:137], off
	global_load_dwordx4 v[150:153], v[132:133], off
	v_lshl_add_u64 v[132:133], v[212:213], 1, s[26:27]
	v_lshl_add_u64 v[130:131], v[132:133], 0, v[130:131]
	global_load_dwordx4 v[142:145], v[130:131], off
	v_lshl_add_u64 v[130:131], v[132:133], 0, v[134:135]
	v_add_u32_e32 v220, 0x80, v218
	global_load_dwordx4 v[134:137], v[130:131], off
	v_ashrrev_i32_e32 v130, 5, v220
	v_and_b32_e32 v146, -8, v130
	v_add_u32_e32 v130, s0, v146
	v_ashrrev_i32_e32 v131, 31, v130
	v_lshlrev_b64 v[182:183], 17, v[130:131]
	v_lshlrev_b32_e32 v130, 7, v220
	s_movk_i32 s0, 0x4000
	v_and_or_b32 v130, v130, s0, v238
	v_lshlrev_b32_e32 v194, 1, v130
	v_lshl_add_u64 v[130:131], s[26:27], 0, v[194:195]
	v_lshl_add_u64 v[132:133], v[130:131], 0, v[182:183]
	global_load_dwordx4 v[138:141], v[132:133], off
	v_add_u32_e32 v132, s1, v146
	v_ashrrev_i32_e32 v133, 31, v132
	v_lshlrev_b64 v[190:191], 17, v[132:133]
	v_lshl_add_u64 v[130:131], v[130:131], 0, v[190:191]
	global_load_dwordx4 v[130:133], v[130:131], off
	v_or_b32_e32 v146, 0x2000, v194
	v_mov_b32_e32 v147, v195
	v_lshl_add_u64 v[146:147], s[26:27], 0, v[146:147]
	v_lshl_add_u64 v[148:149], v[146:147], 0, v[182:183]
	global_load_dwordx4 v[166:169], v[148:149], off
	v_lshl_add_u64 v[146:147], v[146:147], 0, v[190:191]
	global_load_dwordx4 v[154:157], v[146:147], off
	v_or_b32_e32 v146, 0x4000, v194
	v_mov_b32_e32 v147, v195
	v_lshl_add_u64 v[146:147], s[26:27], 0, v[146:147]
	v_lshl_add_u64 v[148:149], v[146:147], 0, v[182:183]
	global_load_dwordx4 v[158:161], v[148:149], off
	v_or_b32_e32 v194, 0x6000, v194
	v_lshl_add_u64 v[192:193], s[26:27], 0, v[194:195]
	v_lshl_add_u64 v[146:147], v[146:147], 0, v[190:191]
	v_lshl_add_u64 v[190:191], v[192:193], 0, v[190:191]
	v_lshl_add_u64 v[182:183], v[192:193], 0, v[182:183]
	global_load_dwordx4 v[190:193], v[190:191], off
	s_and_b64 vcc, exec, s[6:7]
	global_load_dwordx4 v[146:149], v[146:147], off
	s_waitcnt vmcnt(0)
	v_lshlrev_b32_e32 v224, 16, v186
	global_load_dwordx4 v[182:185], v[182:183], off
	v_and_b32_e32 v225, 0xffff0000, v186
	v_lshlrev_b32_e32 v186, 16, v187
	v_and_b32_e32 v187, 0xffff0000, v187
	v_pk_mul_f32 v[64:65], v[64:65], v[186:187]
	v_lshlrev_b32_e32 v186, 16, v188
	v_and_b32_e32 v187, 0xffff0000, v188
	v_pk_mul_f32 v[58:59], v[58:59], v[186:187]
	v_lshlrev_b32_e32 v186, 16, v189
	v_and_b32_e32 v187, 0xffff0000, v189
	v_pk_mul_f32 v[60:61], v[60:61], v[186:187]
	v_lshlrev_b32_e32 v186, 16, v178
	v_and_b32_e32 v187, 0xffff0000, v178
	v_lshlrev_b32_e32 v178, 16, v179
	v_and_b32_e32 v179, 0xffff0000, v179
	v_pk_mul_f32 v[32:33], v[32:33], v[178:179]
	v_lshlrev_b32_e32 v178, 16, v180
	v_and_b32_e32 v179, 0xffff0000, v180
	v_pk_mul_f32 v[26:27], v[26:27], v[178:179]
	v_lshlrev_b32_e32 v178, 16, v181
	v_and_b32_e32 v179, 0xffff0000, v181
	v_pk_mul_f32 v[28:29], v[28:29], v[178:179]
	v_lshlrev_b32_e32 v178, 16, v174
	v_and_b32_e32 v179, 0xffff0000, v174
	v_lshlrev_b32_e32 v174, 16, v175
	v_and_b32_e32 v175, 0xffff0000, v175
	v_pk_mul_f32 v[56:57], v[56:57], v[174:175]
	v_lshlrev_b32_e32 v174, 16, v176
	v_and_b32_e32 v175, 0xffff0000, v176
	v_pk_mul_f32 v[50:51], v[50:51], v[174:175]
	v_lshlrev_b32_e32 v174, 16, v177
	v_and_b32_e32 v175, 0xffff0000, v177
	v_pk_mul_f32 v[52:53], v[52:53], v[174:175]
	v_lshlrev_b32_e32 v174, 16, v170
	v_and_b32_e32 v175, 0xffff0000, v170
	v_lshlrev_b32_e32 v170, 16, v171
	v_and_b32_e32 v171, 0xffff0000, v171
	v_pk_mul_f32 v[24:25], v[24:25], v[170:171]
	v_lshlrev_b32_e32 v170, 16, v172
	v_and_b32_e32 v171, 0xffff0000, v172
	v_pk_mul_f32 v[18:19], v[18:19], v[170:171]
	v_lshlrev_b32_e32 v170, 16, v173
	v_and_b32_e32 v171, 0xffff0000, v173
	v_pk_mul_f32 v[20:21], v[20:21], v[170:171]
	v_lshlrev_b32_e32 v170, 16, v162
	v_and_b32_e32 v171, 0xffff0000, v162
	v_lshlrev_b32_e32 v162, 16, v163
	v_and_b32_e32 v163, 0xffff0000, v163
	v_pk_mul_f32 v[48:49], v[48:49], v[162:163]
	v_lshlrev_b32_e32 v162, 16, v164
	v_and_b32_e32 v163, 0xffff0000, v164
	v_pk_mul_f32 v[42:43], v[42:43], v[162:163]
	v_lshlrev_b32_e32 v162, 16, v165
	v_and_b32_e32 v163, 0xffff0000, v165
	v_pk_mul_f32 v[44:45], v[44:45], v[162:163]
	v_lshlrev_b32_e32 v162, 16, v150
	v_and_b32_e32 v163, 0xffff0000, v150
	v_lshlrev_b32_e32 v150, 16, v151
	v_and_b32_e32 v151, 0xffff0000, v151
	v_pk_mul_f32 v[16:17], v[16:17], v[150:151]
	v_lshlrev_b32_e32 v150, 16, v152
	v_and_b32_e32 v151, 0xffff0000, v152
	v_pk_mul_f32 v[10:11], v[10:11], v[150:151]
	v_lshlrev_b32_e32 v150, 16, v153
	v_and_b32_e32 v151, 0xffff0000, v153
	v_pk_mul_f32 v[12:13], v[12:13], v[150:151]
	v_lshlrev_b32_e32 v150, 16, v142
	v_and_b32_e32 v151, 0xffff0000, v142
	v_lshlrev_b32_e32 v142, 16, v143
	v_and_b32_e32 v143, 0xffff0000, v143
	v_pk_mul_f32 v[40:41], v[40:41], v[142:143]
	v_lshlrev_b32_e32 v142, 16, v144
	v_and_b32_e32 v143, 0xffff0000, v144
	v_pk_mul_f32 v[34:35], v[34:35], v[142:143]
	v_lshlrev_b32_e32 v142, 16, v145
	v_and_b32_e32 v143, 0xffff0000, v145
	v_pk_mul_f32 v[36:37], v[36:37], v[142:143]
	v_lshlrev_b32_e32 v142, 16, v134
	v_and_b32_e32 v143, 0xffff0000, v134
	v_lshlrev_b32_e32 v134, 16, v135
	v_and_b32_e32 v135, 0xffff0000, v135
	v_pk_mul_f32 v[8:9], v[8:9], v[134:135]
	v_lshlrev_b32_e32 v134, 16, v136
	v_and_b32_e32 v135, 0xffff0000, v136
	v_pk_mul_f32 v[2:3], v[2:3], v[134:135]
	v_lshlrev_b32_e32 v134, 16, v137
	v_and_b32_e32 v135, 0xffff0000, v137
	v_pk_mul_f32 v[4:5], v[4:5], v[134:135]
	v_lshlrev_b32_e32 v134, 16, v138
	v_and_b32_e32 v135, 0xffff0000, v138
	v_pk_mul_f32 v[66:67], v[66:67], v[134:135]
	v_lshlrev_b32_e32 v134, 16, v139
	v_and_b32_e32 v135, 0xffff0000, v139
	v_pk_mul_f32 v[68:69], v[68:69], v[134:135]
	v_lshlrev_b32_e32 v134, 16, v140
	v_and_b32_e32 v135, 0xffff0000, v140
	v_pk_mul_f32 v[70:71], v[70:71], v[134:135]
	v_lshlrev_b32_e32 v134, 16, v141
	v_and_b32_e32 v135, 0xffff0000, v141
	v_pk_mul_f32 v[72:73], v[72:73], v[134:135]
	v_lshlrev_b32_e32 v134, 16, v130
	v_and_b32_e32 v135, 0xffff0000, v130
	v_lshlrev_b32_e32 v130, 16, v131
	v_and_b32_e32 v131, 0xffff0000, v131
	v_pk_mul_f32 v[100:101], v[100:101], v[130:131]
	v_lshlrev_b32_e32 v130, 16, v132
	v_and_b32_e32 v131, 0xffff0000, v132
	v_pk_mul_f32 v[102:103], v[102:103], v[130:131]
	v_lshlrev_b32_e32 v130, 16, v133
	v_and_b32_e32 v131, 0xffff0000, v133
	v_pk_mul_f32 v[104:105], v[104:105], v[130:131]
	v_lshlrev_b32_e32 v130, 16, v166
	v_and_b32_e32 v131, 0xffff0000, v166
	v_pk_mul_f32 v[74:75], v[74:75], v[130:131]
	v_lshlrev_b32_e32 v130, 16, v167
	v_and_b32_e32 v131, 0xffff0000, v167
	v_pk_mul_f32 v[76:77], v[76:77], v[130:131]
	v_lshlrev_b32_e32 v130, 16, v168
	v_and_b32_e32 v131, 0xffff0000, v168
	v_pk_mul_f32 v[78:79], v[78:79], v[130:131]
	v_lshlrev_b32_e32 v130, 16, v169
	v_and_b32_e32 v131, 0xffff0000, v169
	v_pk_mul_f32 v[80:81], v[80:81], v[130:131]
	v_lshlrev_b32_e32 v130, 16, v154
	v_and_b32_e32 v131, 0xffff0000, v154
	v_pk_mul_f32 v[106:107], v[106:107], v[130:131]
	v_lshlrev_b32_e32 v130, 16, v155
	v_and_b32_e32 v131, 0xffff0000, v155
	v_pk_mul_f32 v[108:109], v[108:109], v[130:131]
	v_lshlrev_b32_e32 v130, 16, v156
	v_and_b32_e32 v131, 0xffff0000, v156
	v_pk_mul_f32 v[110:111], v[110:111], v[130:131]
	v_lshlrev_b32_e32 v130, 16, v157
	v_and_b32_e32 v131, 0xffff0000, v157
	v_pk_mul_f32 v[112:113], v[112:113], v[130:131]
	v_lshlrev_b32_e32 v130, 16, v158
	v_and_b32_e32 v131, 0xffff0000, v158
	v_pk_mul_f32 v[82:83], v[82:83], v[130:131]
	v_lshlrev_b32_e32 v130, 16, v159
	v_and_b32_e32 v131, 0xffff0000, v159
	v_pk_mul_f32 v[84:85], v[84:85], v[130:131]
	v_lshlrev_b32_e32 v130, 16, v160
	v_and_b32_e32 v131, 0xffff0000, v160
	v_pk_mul_f32 v[86:87], v[86:87], v[130:131]
	v_lshlrev_b32_e32 v130, 16, v161
	v_and_b32_e32 v131, 0xffff0000, v161
	v_pk_mul_f32 v[88:89], v[88:89], v[130:131]
	v_lshlrev_b32_e32 v130, 16, v146
	v_and_b32_e32 v131, 0xffff0000, v146
	v_pk_mul_f32 v[114:115], v[114:115], v[130:131]
	v_lshlrev_b32_e32 v130, 16, v147
	v_and_b32_e32 v131, 0xffff0000, v147
	v_pk_mul_f32 v[116:117], v[116:117], v[130:131]
	v_lshlrev_b32_e32 v130, 16, v148
	v_and_b32_e32 v131, 0xffff0000, v148
	v_pk_mul_f32 v[118:119], v[118:119], v[130:131]
	v_lshlrev_b32_e32 v130, 16, v149
	v_and_b32_e32 v131, 0xffff0000, v149
	v_pk_mul_f32 v[120:121], v[120:121], v[130:131]
	s_waitcnt vmcnt(0)
	v_lshlrev_b32_e32 v130, 16, v182
	v_and_b32_e32 v131, 0xffff0000, v182
	v_pk_mul_f32 v[90:91], v[90:91], v[130:131]
	v_lshlrev_b32_e32 v130, 16, v183
	v_and_b32_e32 v131, 0xffff0000, v183
	v_pk_mul_f32 v[92:93], v[92:93], v[130:131]
	v_lshlrev_b32_e32 v130, 16, v184
	v_and_b32_e32 v131, 0xffff0000, v184
	v_pk_mul_f32 v[94:95], v[94:95], v[130:131]
	v_lshlrev_b32_e32 v130, 16, v185
	v_and_b32_e32 v131, 0xffff0000, v185
	v_pk_mul_f32 v[96:97], v[96:97], v[130:131]
	v_lshlrev_b32_e32 v130, 16, v190
	v_and_b32_e32 v131, 0xffff0000, v190
	v_pk_mul_f32 v[122:123], v[122:123], v[130:131]
	v_lshlrev_b32_e32 v130, 16, v191
	v_and_b32_e32 v131, 0xffff0000, v191
	v_pk_mul_f32 v[124:125], v[124:125], v[130:131]
	v_lshlrev_b32_e32 v130, 16, v192
	v_and_b32_e32 v131, 0xffff0000, v192
	v_pk_mul_f32 v[126:127], v[126:127], v[130:131]
	v_lshlrev_b32_e32 v130, 16, v193
	v_and_b32_e32 v131, 0xffff0000, v193
	v_pk_mul_f32 v[62:63], v[62:63], v[224:225]
	v_pk_mul_f32 v[30:31], v[30:31], v[186:187]
	v_pk_mul_f32 v[54:55], v[54:55], v[178:179]
	v_pk_mul_f32 v[22:23], v[22:23], v[174:175]
	v_pk_mul_f32 v[46:47], v[46:47], v[170:171]
	v_pk_mul_f32 v[14:15], v[14:15], v[162:163]
	v_pk_mul_f32 v[38:39], v[38:39], v[150:151]
	v_pk_mul_f32 v[6:7], v[6:7], v[142:143]
	v_pk_mul_f32 v[98:99], v[98:99], v[134:135]
	v_pk_mul_f32 v[128:129], v[128:129], v[130:131]
	s_cbranch_vccz .LBB0_1335
	v_lshl_or_b32 v134, s79, 8, v239
	v_ashrrev_i32_e32 v219, 31, v218
	v_lshlrev_b64 v[130:131], 11, v[218:219]
	v_ashrrev_i32_e32 v135, 31, v134
	v_lshl_add_u64 v[136:137], s[8:9], 0, v[130:131]
	v_lshlrev_b64 v[134:135], 1, v[134:135]
	v_cvt_pk_bf16_f32 v130, v62, v63
	v_cvt_pk_bf16_f32 v131, v64, v65
	v_cvt_pk_bf16_f32 v132, v58, v59
	v_cvt_pk_bf16_f32 v133, v60, v61
	v_lshl_add_u64 v[136:137], v[136:137], 0, v[134:135]
	global_store_dwordx4 v[136:137], v[130:133], off
	v_ashrrev_i32_e32 v221, 31, v220
	s_mov_b64 s[0:1], 0x48000
	v_cvt_pk_bf16_f32 v130, v30, v31
	v_cvt_pk_bf16_f32 v131, v32, v33
	v_cvt_pk_bf16_f32 v132, v26, v27
	v_cvt_pk_bf16_f32 v133, v28, v29
	global_store_dwordx4 v[136:137], v[130:133], off offset:256
	s_nop 1
	v_or_b32_e32 v130, 16, v218
	v_ashrrev_i32_e32 v131, 31, v130
	v_lshlrev_b64 v[130:131], 11, v[130:131]
	v_lshl_add_u64 v[138:139], s[8:9], 0, v[130:131]
	v_cvt_pk_bf16_f32 v130, v54, v55
	v_cvt_pk_bf16_f32 v131, v56, v57
	v_cvt_pk_bf16_f32 v132, v50, v51
	v_cvt_pk_bf16_f32 v133, v52, v53
	v_lshl_add_u64 v[138:139], v[138:139], 0, v[134:135]
	global_store_dwordx4 v[138:139], v[130:133], off
	s_nop 1
	v_cvt_pk_bf16_f32 v130, v22, v23
	v_cvt_pk_bf16_f32 v131, v24, v25
	v_cvt_pk_bf16_f32 v132, v18, v19
	v_cvt_pk_bf16_f32 v133, v20, v21
	global_store_dwordx4 v[138:139], v[130:133], off offset:256
	s_nop 1
	v_or_b32_e32 v130, 32, v218
	v_ashrrev_i32_e32 v131, 31, v130
	v_lshlrev_b64 v[130:131], 11, v[130:131]
	v_lshl_add_u64 v[138:139], s[8:9], 0, v[130:131]
	v_cvt_pk_bf16_f32 v130, v46, v47
	v_cvt_pk_bf16_f32 v131, v48, v49
	v_cvt_pk_bf16_f32 v132, v42, v43
	v_cvt_pk_bf16_f32 v133, v44, v45
	v_lshl_add_u64 v[138:139], v[138:139], 0, v[134:135]
	global_store_dwordx4 v[138:139], v[130:133], off
	s_nop 1
	v_cvt_pk_bf16_f32 v130, v14, v15
	v_cvt_pk_bf16_f32 v131, v16, v17
	v_cvt_pk_bf16_f32 v132, v10, v11
	v_cvt_pk_bf16_f32 v133, v12, v13
	global_store_dwordx4 v[138:139], v[130:133], off offset:256
	s_nop 1
	v_or_b32_e32 v130, 48, v218
	v_ashrrev_i32_e32 v131, 31, v130
	v_lshlrev_b64 v[130:131], 11, v[130:131]
	v_lshl_add_u64 v[138:139], s[8:9], 0, v[130:131]
	v_cvt_pk_bf16_f32 v130, v38, v39
	v_cvt_pk_bf16_f32 v131, v40, v41
	v_cvt_pk_bf16_f32 v132, v34, v35
	v_cvt_pk_bf16_f32 v133, v36, v37
	v_lshl_add_u64 v[138:139], v[138:139], 0, v[134:135]
	global_store_dwordx4 v[138:139], v[130:133], off
	s_nop 1
	v_cvt_pk_bf16_f32 v130, v6, v7
	v_cvt_pk_bf16_f32 v131, v8, v9
	v_cvt_pk_bf16_f32 v132, v2, v3
	v_cvt_pk_bf16_f32 v133, v4, v5
	global_store_dwordx4 v[138:139], v[130:133], off offset:256
	s_nop 1
	v_lshlrev_b64 v[130:131], 11, v[220:221]
	v_lshl_add_u64 v[138:139], s[8:9], 0, v[130:131]
	v_cvt_pk_bf16_f32 v130, v66, v67
	v_cvt_pk_bf16_f32 v131, v68, v69
	v_cvt_pk_bf16_f32 v132, v70, v71
	v_cvt_pk_bf16_f32 v133, v72, v73
	v_lshl_add_u64 v[134:135], v[138:139], 0, v[134:135]
	global_store_dwordx4 v[134:135], v[130:133], off
	s_nop 1
	v_cvt_pk_bf16_f32 v130, v98, v99
	v_cvt_pk_bf16_f32 v131, v100, v101
	v_cvt_pk_bf16_f32 v132, v102, v103
	v_cvt_pk_bf16_f32 v133, v104, v105
	global_store_dwordx4 v[134:135], v[130:133], off offset:256
	v_lshl_add_u64 v[134:135], v[136:137], 0, s[0:1]
	s_mov_b32 s0, 0x48000
	v_add_co_u32_e32 v138, vcc, s0, v136
	v_cvt_pk_bf16_f32 v130, v74, v75
	v_cvt_pk_bf16_f32 v131, v76, v77
	v_cvt_pk_bf16_f32 v132, v78, v79
	v_cvt_pk_bf16_f32 v133, v80, v81
	v_addc_co_u32_e32 v139, vcc, 0, v137, vcc
	global_store_dwordx4 v[138:139], v[130:133], off
	s_mov_b64 s[0:1], 0x50000
	s_nop 0
	v_cvt_pk_bf16_f32 v130, v106, v107
	v_cvt_pk_bf16_f32 v131, v108, v109
	v_cvt_pk_bf16_f32 v132, v110, v111
	v_cvt_pk_bf16_f32 v133, v112, v113
	global_store_dwordx4 v[134:135], v[130:133], off offset:256
	v_lshl_add_u64 v[134:135], v[136:137], 0, s[0:1]
	s_mov_b32 s0, 0x50000
	v_add_co_u32_e32 v138, vcc, s0, v136
	v_cvt_pk_bf16_f32 v130, v82, v83
	v_cvt_pk_bf16_f32 v131, v84, v85
	v_cvt_pk_bf16_f32 v132, v86, v87
	v_cvt_pk_bf16_f32 v133, v88, v89
	v_addc_co_u32_e32 v139, vcc, 0, v137, vcc
	global_store_dwordx4 v[138:139], v[130:133], off
	s_mov_b64 s[0:1], 0x58000
	s_nop 0
	v_cvt_pk_bf16_f32 v130, v114, v115
	v_cvt_pk_bf16_f32 v131, v116, v117
	v_cvt_pk_bf16_f32 v132, v118, v119
	v_cvt_pk_bf16_f32 v133, v120, v121
	global_store_dwordx4 v[134:135], v[130:133], off offset:256
	v_lshl_add_u64 v[134:135], v[136:137], 0, s[0:1]
	s_mov_b32 s0, 0x58000
	v_add_co_u32_e32 v136, vcc, s0, v136
	v_cvt_pk_bf16_f32 v130, v90, v91
	v_cvt_pk_bf16_f32 v131, v92, v93
	v_cvt_pk_bf16_f32 v132, v94, v95
	v_cvt_pk_bf16_f32 v133, v96, v97
	v_addc_co_u32_e32 v137, vcc, 0, v137, vcc
	global_store_dwordx4 v[136:137], v[130:133], off
	s_nop 1
	v_cvt_pk_bf16_f32 v130, v122, v123
	v_cvt_pk_bf16_f32 v131, v124, v125
	v_cvt_pk_bf16_f32 v132, v126, v127
	v_cvt_pk_bf16_f32 v133, v128, v129
	global_store_dwordx4 v[134:135], v[130:133], off offset:256

.LBB0_1765:
	s_add_u32 s0, s24, 0xfffc0080
	s_addc_u32 s1, s25, -1
	s_add_i32 s33, 0, 0x10000
	s_cmp_eq_u32 s82, 12
	s_cselect_b32 s29, s19, s1
	s_cselect_b32 s28, s76, s0
	s_cselect_b32 s27, s15, s79
	s_cselect_b32 s26, s77, s78
	s_add_i32 m0, s13, 0xc000
	ds_read_b128 v[160:163], v143
	ds_read_b128 v[164:167], v143 offset:1024
	ds_read_b128 v[168:171], v143 offset:2048
	ds_read_b128 v[172:175], v143 offset:3072
	ds_read_b128 v[176:179], v143 offset:4096
	ds_read_b128 v[180:183], v143 offset:5120
	ds_read_b128 v[184:187], v143 offset:6144
	ds_read_b128 v[188:191], v143 offset:7168
	global_load_lds_dwordx4 v136, s[24:25]
	s_add_i32 m0, s13, 0xe000
	s_nop 0
	global_load_lds_dwordx4 v138, s[24:25]
	s_waitcnt lgkmcnt(8)
	s_barrier
	s_waitcnt lgkmcnt(0)
	v_mfma_f32_16x16x32_bf16 v[126:129], v[144:147], v[160:163], v[126:129]
	v_mfma_f32_16x16x32_bf16 v[122:125], v[152:155], v[160:163], v[122:125]
	v_mfma_f32_16x16x32_bf16 v[118:121], v[144:147], v[168:171], v[118:121]
	v_mfma_f32_16x16x32_bf16 v[114:117], v[152:155], v[168:171], v[114:117]
	v_mfma_f32_16x16x32_bf16 v[102:105], v[144:147], v[176:179], v[102:105]
	v_mfma_f32_16x16x32_bf16 v[98:101], v[152:155], v[176:179], v[98:101]
	v_mfma_f32_16x16x32_bf16 v[86:89], v[144:147], v[184:187], v[86:89]
	v_mfma_f32_16x16x32_bf16 v[82:85], v[152:155], v[184:187], v[82:85]
	v_mfma_f32_16x16x32_bf16 v[126:129], v[148:151], v[164:167], v[126:129]
	v_mfma_f32_16x16x32_bf16 v[122:125], v[156:159], v[164:167], v[122:125]
	v_mfma_f32_16x16x32_bf16 v[118:121], v[148:151], v[172:175], v[118:121]
	v_mfma_f32_16x16x32_bf16 v[114:117], v[156:159], v[172:175], v[114:117]
	v_mfma_f32_16x16x32_bf16 v[102:105], v[148:151], v[180:183], v[102:105]
	v_mfma_f32_16x16x32_bf16 v[98:101], v[156:159], v[180:183], v[98:101]
	v_mfma_f32_16x16x32_bf16 v[86:89], v[148:151], v[188:191], v[86:89]
	v_mfma_f32_16x16x32_bf16 v[82:85], v[156:159], v[188:191], v[82:85]
	s_barrier
	s_add_i32 s36, 0, 0x14000
	v_add_u32_e32 v192, s36, v141
	s_add_i32 s0, s33, s64
	ds_read_b128 v[198:201], v192
	ds_read_b128 v[202:205], v192 offset:1024
	ds_read_b128 v[206:209], v192 offset:2048
	ds_read_b128 v[210:213], v192 offset:3072
	v_lshl_add_u64 v[192:193], s[26:27], 0, v[194:195]
	s_mov_b32 m0, s0
	v_lshl_add_u64 v[214:215], s[26:27], 0, v[130:131]
	global_load_lds_dwordx4 v[192:193], off
	s_add_i32 m0, s0, 0x2000
	s_nop 0
	global_load_lds_dwordx4 v[214:215], off
	s_barrier
	s_waitcnt lgkmcnt(0)
	v_mfma_f32_16x16x32_bf16 v[110:113], v[198:201], v[160:163], v[110:113]
	v_mfma_f32_16x16x32_bf16 v[106:109], v[206:209], v[160:163], v[106:109]
	v_mfma_f32_16x16x32_bf16 v[94:97], v[198:201], v[168:171], v[94:97]
	v_mfma_f32_16x16x32_bf16 v[90:93], v[206:209], v[168:171], v[90:93]
	v_mfma_f32_16x16x32_bf16 v[78:81], v[198:201], v[176:179], v[78:81]
	v_mfma_f32_16x16x32_bf16 v[74:77], v[206:209], v[176:179], v[74:77]
	v_mfma_f32_16x16x32_bf16 v[70:73], v[198:201], v[184:187], v[70:73]
	v_mfma_f32_16x16x32_bf16 v[66:69], v[206:209], v[184:187], v[66:69]
	v_mfma_f32_16x16x32_bf16 v[110:113], v[202:205], v[164:167], v[110:113]
	v_mfma_f32_16x16x32_bf16 v[106:109], v[210:213], v[164:167], v[106:109]
	v_mfma_f32_16x16x32_bf16 v[94:97], v[202:205], v[172:175], v[94:97]
	v_mfma_f32_16x16x32_bf16 v[90:93], v[210:213], v[172:175], v[90:93]
	v_mfma_f32_16x16x32_bf16 v[78:81], v[202:205], v[180:183], v[78:81]
	v_mfma_f32_16x16x32_bf16 v[74:77], v[210:213], v[180:183], v[74:77]
	v_mfma_f32_16x16x32_bf16 v[70:73], v[202:205], v[188:191], v[70:73]
	v_mfma_f32_16x16x32_bf16 v[66:69], v[210:213], v[188:191], v[66:69]
	s_mov_b32 m0, s13
	v_lshl_add_u64 v[216:217], s[28:29], 0, v[134:135]
	s_barrier
	ds_read_b128 v[160:163], v143 offset:16384
	ds_read_b128 v[164:167], v143 offset:17408
	ds_read_b128 v[168:171], v143 offset:18432
	ds_read_b128 v[172:175], v143 offset:19456
	ds_read_b128 v[176:179], v143 offset:20480
	ds_read_b128 v[180:183], v143 offset:21504
	ds_read_b128 v[184:187], v143 offset:22528
	ds_read_b128 v[188:191], v143 offset:23552
	global_load_lds_dwordx4 v[216:217], off
	v_lshl_add_u64 v[218:219], s[28:29], 0, v[132:133]
	s_mov_b32 m0, s68
	s_nop 0
	global_load_lds_dwordx4 v[218:219], off
	s_waitcnt vmcnt(10)
	s_barrier
	s_waitcnt lgkmcnt(0)
	v_mfma_f32_16x16x32_bf16 v[62:65], v[144:147], v[160:163], v[62:65]
	v_mfma_f32_16x16x32_bf16 v[58:61], v[152:155], v[160:163], v[58:61]
	v_mfma_f32_16x16x32_bf16 v[54:57], v[144:147], v[168:171], v[54:57]
	v_mfma_f32_16x16x32_bf16 v[50:53], v[152:155], v[168:171], v[50:53]
	v_mfma_f32_16x16x32_bf16 v[38:41], v[144:147], v[176:179], v[38:41]
	v_mfma_f32_16x16x32_bf16 v[34:37], v[152:155], v[176:179], v[34:37]
	v_mfma_f32_16x16x32_bf16 v[22:25], v[144:147], v[184:187], v[22:25]
	v_mfma_f32_16x16x32_bf16 v[18:21], v[152:155], v[184:187], v[18:21]
	v_mfma_f32_16x16x32_bf16 v[62:65], v[148:151], v[164:167], v[62:65]
	v_mfma_f32_16x16x32_bf16 v[58:61], v[156:159], v[164:167], v[58:61]
	v_mfma_f32_16x16x32_bf16 v[54:57], v[148:151], v[172:175], v[54:57]
	v_mfma_f32_16x16x32_bf16 v[50:53], v[156:159], v[172:175], v[50:53]
	v_mfma_f32_16x16x32_bf16 v[38:41], v[148:151], v[180:183], v[38:41]
	v_mfma_f32_16x16x32_bf16 v[34:37], v[156:159], v[180:183], v[34:37]
	v_mfma_f32_16x16x32_bf16 v[22:25], v[148:151], v[188:191], v[22:25]
	v_mfma_f32_16x16x32_bf16 v[18:21], v[156:159], v[188:191], v[18:21]
	s_barrier
	s_add_u32 s0, s26, 0x40000
	s_addc_u32 s1, s27, 0
	s_add_i32 s33, s36, s64
	s_mov_b32 m0, s33
	s_nop 0
	global_load_lds_dwordx4 v194, s[0:1]
	s_add_i32 m0, s33, 0x2000
	s_nop 0
	global_load_lds_dwordx4 v130, s[0:1]
	v_add_u32_e32 v156, 0x18000, v141
	ds_read_b128 v[144:147], v156
	ds_read_b128 v[148:151], v156 offset:1024
	ds_read_b128 v[152:155], v156 offset:2048
	ds_read_b128 v[156:159], v156 offset:3072
	s_waitcnt vmcnt(6)
	s_barrier
	v_mfma_f32_16x16x32_bf16 v[46:49], v[198:201], v[160:163], v[46:49]
	v_mfma_f32_16x16x32_bf16 v[42:45], v[206:209], v[160:163], v[42:45]
	v_mfma_f32_16x16x32_bf16 v[30:33], v[198:201], v[168:171], v[30:33]
	v_mfma_f32_16x16x32_bf16 v[26:29], v[206:209], v[168:171], v[26:29]
	v_mfma_f32_16x16x32_bf16 v[14:17], v[198:201], v[176:179], v[14:17]
	v_mfma_f32_16x16x32_bf16 v[10:13], v[206:209], v[176:179], v[10:13]
	v_mfma_f32_16x16x32_bf16 v[6:9], v[198:201], v[184:187], v[6:9]
	v_mfma_f32_16x16x32_bf16 v[2:5], v[206:209], v[184:187], v[2:5]
	v_mfma_f32_16x16x32_bf16 v[46:49], v[202:205], v[164:167], v[46:49]
	v_mfma_f32_16x16x32_bf16 v[42:45], v[210:213], v[164:167], v[42:45]
	v_mfma_f32_16x16x32_bf16 v[30:33], v[202:205], v[172:175], v[30:33]
	v_mfma_f32_16x16x32_bf16 v[26:29], v[210:213], v[172:175], v[26:29]
	v_mfma_f32_16x16x32_bf16 v[14:17], v[202:205], v[180:183], v[14:17]
	v_mfma_f32_16x16x32_bf16 v[10:13], v[210:213], v[180:183], v[10:13]
	v_mfma_f32_16x16x32_bf16 v[6:9], v[202:205], v[188:191], v[6:9]
	v_mfma_f32_16x16x32_bf16 v[2:5], v[210:213], v[188:191], v[2:5]
	s_add_i32 s33, 0, 0x18000
	s_barrier
	s_add_u32 s0, s28, 0x40000
	s_addc_u32 s1, s29, 0
	s_mov_b32 m0, s69
	ds_read_b128 v[160:163], v143 offset:32768
	ds_read_b128 v[164:167], v143 offset:33792
	ds_read_b128 v[168:171], v143 offset:34816
	ds_read_b128 v[172:175], v143 offset:35840
	ds_read_b128 v[176:179], v143 offset:36864
	ds_read_b128 v[180:183], v143 offset:37888
	ds_read_b128 v[184:187], v143 offset:38912
	ds_read_b128 v[188:191], v143 offset:39936
	global_load_lds_dwordx4 v134, s[0:1]
	s_mov_b32 m0, s70
	s_nop 0
	global_load_lds_dwordx4 v132, s[0:1]
	s_waitcnt lgkmcnt(8)
	s_barrier
	s_waitcnt lgkmcnt(0)
	v_mfma_f32_16x16x32_bf16 v[126:129], v[144:147], v[160:163], v[126:129]
	v_mfma_f32_16x16x32_bf16 v[122:125], v[152:155], v[160:163], v[122:125]
	v_mfma_f32_16x16x32_bf16 v[118:121], v[144:147], v[168:171], v[118:121]
	v_mfma_f32_16x16x32_bf16 v[114:117], v[152:155], v[168:171], v[114:117]
	v_mfma_f32_16x16x32_bf16 v[102:105], v[144:147], v[176:179], v[102:105]
	v_mfma_f32_16x16x32_bf16 v[98:101], v[152:155], v[176:179], v[98:101]
	v_mfma_f32_16x16x32_bf16 v[86:89], v[144:147], v[184:187], v[86:89]
	v_mfma_f32_16x16x32_bf16 v[82:85], v[152:155], v[184:187], v[82:85]
	v_mfma_f32_16x16x32_bf16 v[126:129], v[148:151], v[164:167], v[126:129]
	v_mfma_f32_16x16x32_bf16 v[122:125], v[156:159], v[164:167], v[122:125]
	v_mfma_f32_16x16x32_bf16 v[118:121], v[148:151], v[172:175], v[118:121]
	v_mfma_f32_16x16x32_bf16 v[114:117], v[156:159], v[172:175], v[114:117]
	v_mfma_f32_16x16x32_bf16 v[102:105], v[148:151], v[180:183], v[102:105]
	v_mfma_f32_16x16x32_bf16 v[98:101], v[156:159], v[180:183], v[98:101]
	v_mfma_f32_16x16x32_bf16 v[86:89], v[148:151], v[188:191], v[86:89]
	v_mfma_f32_16x16x32_bf16 v[82:85], v[156:159], v[188:191], v[82:85]
	s_barrier
	s_add_i32 s28, 0, 0x1c000
	s_add_i32 s0, s33, s64
	v_add_u32_e32 v196, s28, v141
	v_lshl_add_u64 v[192:193], v[192:193], 0, s[54:55]
	s_mov_b32 m0, s0
	ds_read_b128 v[198:201], v196
	ds_read_b128 v[202:205], v196 offset:1024
	ds_read_b128 v[206:209], v196 offset:2048
	ds_read_b128 v[210:213], v196 offset:3072
	global_load_lds_dwordx4 v[192:193], off
	v_lshl_add_u64 v[192:193], v[214:215], 0, s[54:55]
	s_add_i32 m0, s0, 0x2000
	s_nop 0
	global_load_lds_dwordx4 v[192:193], off
	s_barrier
	s_waitcnt lgkmcnt(0)
	v_mfma_f32_16x16x32_bf16 v[110:113], v[198:201], v[160:163], v[110:113]
	v_mfma_f32_16x16x32_bf16 v[106:109], v[206:209], v[160:163], v[106:109]
	v_mfma_f32_16x16x32_bf16 v[94:97], v[198:201], v[168:171], v[94:97]
	v_mfma_f32_16x16x32_bf16 v[90:93], v[206:209], v[168:171], v[90:93]
	v_mfma_f32_16x16x32_bf16 v[78:81], v[198:201], v[176:179], v[78:81]
	v_mfma_f32_16x16x32_bf16 v[74:77], v[206:209], v[176:179], v[74:77]
	v_mfma_f32_16x16x32_bf16 v[70:73], v[198:201], v[184:187], v[70:73]
	v_mfma_f32_16x16x32_bf16 v[66:69], v[206:209], v[184:187], v[66:69]
	v_mfma_f32_16x16x32_bf16 v[110:113], v[202:205], v[164:167], v[110:113]
	v_mfma_f32_16x16x32_bf16 v[106:109], v[210:213], v[164:167], v[106:109]
	v_mfma_f32_16x16x32_bf16 v[94:97], v[202:205], v[172:175], v[94:97]
	v_mfma_f32_16x16x32_bf16 v[90:93], v[210:213], v[172:175], v[90:93]
	v_mfma_f32_16x16x32_bf16 v[78:81], v[202:205], v[180:183], v[78:81]
	v_mfma_f32_16x16x32_bf16 v[74:77], v[210:213], v[180:183], v[74:77]
	v_mfma_f32_16x16x32_bf16 v[70:73], v[202:205], v[188:191], v[70:73]
	v_mfma_f32_16x16x32_bf16 v[66:69], v[210:213], v[188:191], v[66:69]
	s_mov_b32 m0, s71
	v_lshl_add_u64 v[192:193], v[216:217], 0, s[54:55]
	s_barrier
	ds_read_b128 v[160:163], v143 offset:49152
	ds_read_b128 v[164:167], v143 offset:50176
	ds_read_b128 v[168:171], v143 offset:51200
	ds_read_b128 v[172:175], v143 offset:52224
	ds_read_b128 v[176:179], v143 offset:53248
	ds_read_b128 v[180:183], v143 offset:54272
	ds_read_b128 v[184:187], v143 offset:55296
	ds_read_b128 v[188:191], v143 offset:56320
	global_load_lds_dwordx4 v[192:193], off
	v_lshl_add_u64 v[192:193], v[218:219], 0, s[54:55]
	s_mov_b32 m0, s72
	s_nop 0
	global_load_lds_dwordx4 v[192:193], off
	s_waitcnt vmcnt(10)
	s_barrier
	s_waitcnt lgkmcnt(0)
	v_mfma_f32_16x16x32_bf16 v[62:65], v[144:147], v[160:163], v[62:65]
	v_mfma_f32_16x16x32_bf16 v[58:61], v[152:155], v[160:163], v[58:61]
	v_mfma_f32_16x16x32_bf16 v[54:57], v[144:147], v[168:171], v[54:57]
	v_mfma_f32_16x16x32_bf16 v[50:53], v[152:155], v[168:171], v[50:53]
	v_mfma_f32_16x16x32_bf16 v[38:41], v[144:147], v[176:179], v[38:41]
	v_mfma_f32_16x16x32_bf16 v[34:37], v[152:155], v[176:179], v[34:37]
	v_mfma_f32_16x16x32_bf16 v[22:25], v[144:147], v[184:187], v[22:25]
	v_mfma_f32_16x16x32_bf16 v[18:21], v[152:155], v[184:187], v[18:21]
	v_mfma_f32_16x16x32_bf16 v[62:65], v[148:151], v[164:167], v[62:65]
	v_mfma_f32_16x16x32_bf16 v[58:61], v[156:159], v[164:167], v[58:61]
	v_mfma_f32_16x16x32_bf16 v[54:57], v[148:151], v[172:175], v[54:57]
	v_mfma_f32_16x16x32_bf16 v[50:53], v[156:159], v[172:175], v[50:53]
	v_mfma_f32_16x16x32_bf16 v[38:41], v[148:151], v[180:183], v[38:41]
	v_mfma_f32_16x16x32_bf16 v[34:37], v[156:159], v[180:183], v[34:37]
	v_mfma_f32_16x16x32_bf16 v[22:25], v[148:151], v[188:191], v[22:25]
	v_mfma_f32_16x16x32_bf16 v[18:21], v[156:159], v[188:191], v[18:21]
	s_barrier
	s_add_u32 s0, s26, 0x40080
	s_addc_u32 s1, s27, 0
	s_add_i32 s26, s28, s64
	s_mov_b32 m0, s26
	s_nop 0
	global_load_lds_dwordx4 v194, s[0:1]
	s_add_i32 m0, s26, 0x2000
	s_nop 0
	global_load_lds_dwordx4 v130, s[0:1]
	v_add_u32_e32 v156, 0x10000, v141
	ds_read_b128 v[144:147], v156
	ds_read_b128 v[148:151], v156 offset:1024
	ds_read_b128 v[152:155], v156 offset:2048
	ds_read_b128 v[156:159], v156 offset:3072
	s_waitcnt vmcnt(6)
	s_barrier
	v_mfma_f32_16x16x32_bf16 v[46:49], v[198:201], v[160:163], v[46:49]
	v_mfma_f32_16x16x32_bf16 v[42:45], v[206:209], v[160:163], v[42:45]
	v_mfma_f32_16x16x32_bf16 v[30:33], v[198:201], v[168:171], v[30:33]
	v_mfma_f32_16x16x32_bf16 v[26:29], v[206:209], v[168:171], v[26:29]
	v_mfma_f32_16x16x32_bf16 v[14:17], v[198:201], v[176:179], v[14:17]
	v_mfma_f32_16x16x32_bf16 v[10:13], v[206:209], v[176:179], v[10:13]
	v_mfma_f32_16x16x32_bf16 v[6:9], v[198:201], v[184:187], v[6:9]
	v_mfma_f32_16x16x32_bf16 v[2:5], v[206:209], v[184:187], v[2:5]
	v_mfma_f32_16x16x32_bf16 v[46:49], v[202:205], v[164:167], v[46:49]
	v_mfma_f32_16x16x32_bf16 v[42:45], v[210:213], v[164:167], v[42:45]
	v_mfma_f32_16x16x32_bf16 v[30:33], v[202:205], v[172:175], v[30:33]
	v_mfma_f32_16x16x32_bf16 v[26:29], v[210:213], v[172:175], v[26:29]
	v_mfma_f32_16x16x32_bf16 v[14:17], v[202:205], v[180:183], v[14:17]
	v_mfma_f32_16x16x32_bf16 v[10:13], v[210:213], v[180:183], v[10:13]
	v_mfma_f32_16x16x32_bf16 v[6:9], v[202:205], v[188:191], v[6:9]
	v_mfma_f32_16x16x32_bf16 v[2:5], v[210:213], v[188:191], v[2:5]
	s_add_i32 s82, s82, 2
	s_add_u32 s24, s24, 0x100
	s_addc_u32 s25, s25, 0
	s_add_u32 s78, s78, 0x100
	s_addc_u32 s79, s79, 0
	s_cmp_gt_u32 s82, 13
	s_barrier
	s_cbranch_scc0 .LBB0_1765
	s_waitcnt lgkmcnt(0)
	v_lshl_add_u32 v144, s12, 8, v1
	v_lshl_or_b32 v146, s75, 8, v142
	v_ashrrev_i32_e32 v145, 31, v144
	v_lshlrev_b64 v[148:149], 11, v[144:145]
	v_ashrrev_i32_e32 v147, 31, v146
	v_lshl_add_u64 v[148:149], s[10:11], 0, v[148:149]
	v_cvt_pk_bf16_f32 v126, v126, v127
	v_cvt_pk_bf16_f32 v127, v128, v129
	v_cvt_pk_bf16_f32 v128, v122, v123
	v_lshlrev_b64 v[122:123], 1, v[146:147]
	v_cvt_pk_bf16_f32 v129, v124, v125
	v_lshl_add_u64 v[124:125], v[148:149], 0, v[122:123]
	s_mov_b64 s[0:1], 0x40000
	v_cvt_pk_bf16_f32 v62, v62, v63
	v_cvt_pk_bf16_f32 v63, v64, v65
	v_cvt_pk_bf16_f32 v64, v58, v59
	v_lshl_add_u64 v[58:59], v[124:125], 0, s[0:1]
	s_mov_b32 s0, 0x40000
	v_cvt_pk_bf16_f32 v110, v110, v111
	v_cvt_pk_bf16_f32 v111, v112, v113
	v_cvt_pk_bf16_f32 v112, v106, v107
	v_or_b32_e32 v106, 16, v144
	v_cvt_pk_bf16_f32 v65, v60, v61
	v_add_co_u32_e32 v60, vcc, s0, v124
	v_cvt_pk_bf16_f32 v46, v46, v47
	v_cvt_pk_bf16_f32 v47, v48, v49
	v_cvt_pk_bf16_f32 v48, v42, v43
	v_cvt_pk_bf16_f32 v49, v44, v45
	s_mov_b64 s[0:1], 0x48000
	v_ashrrev_i32_e32 v107, 31, v106
	v_addc_co_u32_e32 v61, vcc, 0, v125, vcc
	global_store_dwordx4 v[58:59], v[46:49], off offset:256
	v_cvt_pk_bf16_f32 v113, v108, v109
	v_lshlrev_b64 v[106:107], 11, v[106:107]
	v_lshl_add_u64 v[46:47], v[124:125], 0, s[0:1]
	s_mov_b32 s0, 0x48000
	v_cvt_pk_bf16_f32 v94, v94, v95
	v_cvt_pk_bf16_f32 v95, v96, v97
	v_cvt_pk_bf16_f32 v96, v90, v91
	v_or_b32_e32 v90, 32, v144
	v_add_co_u32_e32 v48, vcc, s0, v124
	v_cvt_pk_bf16_f32 v30, v30, v31
	v_cvt_pk_bf16_f32 v31, v32, v33
	v_cvt_pk_bf16_f32 v32, v26, v27
	v_cvt_pk_bf16_f32 v33, v28, v29
	s_mov_b64 s[0:1], 0x50000
	global_store_dwordx4 v[124:125], v[110:113], off offset:256
	v_ashrrev_i32_e32 v91, 31, v90
	v_addc_co_u32_e32 v49, vcc, 0, v125, vcc
	v_lshl_add_u64 v[110:111], s[10:11], 0, v[106:107]
	global_store_dwordx4 v[46:47], v[30:33], off offset:256
	v_lshl_add_u64 v[110:111], v[110:111], 0, v[122:123]
	v_cvt_pk_bf16_f32 v97, v92, v93
	v_lshl_add_u64 v[30:31], v[124:125], 0, s[0:1]
	s_mov_b32 s0, 0x50000
	v_lshlrev_b64 v[90:91], 11, v[90:91]
	v_cvt_pk_bf16_f32 v78, v78, v79
	v_cvt_pk_bf16_f32 v79, v80, v81
	v_cvt_pk_bf16_f32 v80, v74, v75
	v_or_b32_e32 v74, 48, v144
	v_add_co_u32_e32 v32, vcc, s0, v124
	v_cvt_pk_bf16_f32 v14, v14, v15
	v_cvt_pk_bf16_f32 v15, v16, v17
	v_cvt_pk_bf16_f32 v16, v10, v11
	v_cvt_pk_bf16_f32 v17, v12, v13
	s_mov_b64 s[0:1], 0x58000
	global_store_dwordx4 v[110:111], v[94:97], off offset:256
	v_ashrrev_i32_e32 v75, 31, v74
	v_addc_co_u32_e32 v33, vcc, 0, v125, vcc
	v_lshl_add_u64 v[94:95], s[10:11], 0, v[90:91]
	global_store_dwordx4 v[30:31], v[14:17], off offset:256
	v_lshl_add_u64 v[94:95], v[94:95], 0, v[122:123]
	v_cvt_pk_bf16_f32 v81, v76, v77
	v_lshl_add_u64 v[14:15], v[124:125], 0, s[0:1]
	s_mov_b32 s0, 0x58000
	v_lshlrev_b64 v[74:75], 11, v[74:75]
	v_add_co_u32_e32 v16, vcc, s0, v124
	global_store_dwordx4 v[94:95], v[78:81], off offset:256
	s_nop 0
	v_addc_co_u32_e32 v17, vcc, 0, v125, vcc
	v_lshl_add_u64 v[78:79], s[10:11], 0, v[74:75]
	v_cvt_pk_bf16_f32 v106, v118, v119
	v_cvt_pk_bf16_f32 v107, v120, v121
	v_cvt_pk_bf16_f32 v108, v114, v115
	v_cvt_pk_bf16_f32 v109, v116, v117
	v_cvt_pk_bf16_f32 v90, v102, v103
	v_cvt_pk_bf16_f32 v91, v104, v105
	v_cvt_pk_bf16_f32 v92, v98, v99
	v_cvt_pk_bf16_f32 v93, v100, v101
	v_cvt_pk_bf16_f32 v74, v86, v87
	v_cvt_pk_bf16_f32 v75, v88, v89
	v_cvt_pk_bf16_f32 v76, v82, v83
	v_cvt_pk_bf16_f32 v77, v84, v85
	v_lshl_add_u64 v[78:79], v[78:79], 0, v[122:123]
	v_cvt_pk_bf16_f32 v70, v70, v71
	v_cvt_pk_bf16_f32 v71, v72, v73
	v_cvt_pk_bf16_f32 v72, v66, v67
	v_cvt_pk_bf16_f32 v73, v68, v69
	v_cvt_pk_bf16_f32 v42, v54, v55
	v_cvt_pk_bf16_f32 v43, v56, v57
	v_cvt_pk_bf16_f32 v44, v50, v51
	v_cvt_pk_bf16_f32 v45, v52, v53
	v_cvt_pk_bf16_f32 v26, v38, v39
	v_cvt_pk_bf16_f32 v27, v40, v41
	v_cvt_pk_bf16_f32 v28, v34, v35
	v_cvt_pk_bf16_f32 v29, v36, v37
	v_cvt_pk_bf16_f32 v10, v22, v23
	v_cvt_pk_bf16_f32 v11, v24, v25
	v_cvt_pk_bf16_f32 v12, v18, v19
	v_cvt_pk_bf16_f32 v13, v20, v21
	v_cvt_pk_bf16_f32 v6, v6, v7
	v_cvt_pk_bf16_f32 v7, v8, v9
	v_cvt_pk_bf16_f32 v8, v2, v3
	v_cvt_pk_bf16_f32 v9, v4, v5
	s_and_b64 vcc, exec, s[4:5]
	s_mov_b32 s75, s14
	s_mov_b32 s12, s18
	s_mov_b64 s[26:27], s[22:23]
	s_mov_b64 s[24:25], s[20:21]
	global_store_dwordx4 v[124:125], v[126:129], off
	global_store_dwordx4 v[110:111], v[106:109], off
	global_store_dwordx4 v[94:95], v[90:93], off
	global_store_dwordx4 v[78:79], v[74:77], off
	global_store_dwordx4 v[78:79], v[70:73], off offset:256
	global_store_dwordx4 v[60:61], v[62:65], off
	global_store_dwordx4 v[48:49], v[42:45], off
	global_store_dwordx4 v[32:33], v[26:29], off
	global_store_dwordx4 v[16:17], v[10:13], off
	global_store_dwordx4 v[14:15], v[6:9], off offset:256
	s_cbranch_vccz .LBB0_1762
	s_waitcnt vmcnt(0)
	s_cmpk_gt_u32 s34, 0xff
	s_cbranch_scc1 .LBB0_1769
	s_barrier

.LBB0_2563:
	s_add_u32 s0, s22, 0xfffe0080
	s_addc_u32 s1, s23, -1
	s_add_i32 s33, 0, 0x10000
	s_cmp_eq_u32 s77, 4
	s_cselect_b32 s27, s11, s1
	s_cselect_b32 s26, s74, s0
	s_cselect_b32 s25, s13, s76
	s_cselect_b32 s24, s15, s75
	s_add_i32 m0, s9, 0xc000
	ds_read_b128 v[160:163], v142
	ds_read_b128 v[164:167], v142 offset:1024
	ds_read_b128 v[168:171], v142 offset:2048
	ds_read_b128 v[172:175], v142 offset:3072
	ds_read_b128 v[176:179], v142 offset:4096
	ds_read_b128 v[180:183], v142 offset:5120
	ds_read_b128 v[184:187], v142 offset:6144
	ds_read_b128 v[188:191], v142 offset:7168
	global_load_lds_dwordx4 v136, s[22:23]
	s_add_i32 m0, s9, 0xe000
	s_nop 0
	global_load_lds_dwordx4 v138, s[22:23]
	s_waitcnt lgkmcnt(8)
	s_barrier
	s_waitcnt lgkmcnt(0)
	v_mfma_f32_16x16x32_bf16 v[126:129], v[144:147], v[160:163], v[126:129]
	v_mfma_f32_16x16x32_bf16 v[122:125], v[152:155], v[160:163], v[122:125]
	v_mfma_f32_16x16x32_bf16 v[118:121], v[144:147], v[168:171], v[118:121]
	v_mfma_f32_16x16x32_bf16 v[114:117], v[152:155], v[168:171], v[114:117]
	v_mfma_f32_16x16x32_bf16 v[102:105], v[144:147], v[176:179], v[102:105]
	v_mfma_f32_16x16x32_bf16 v[98:101], v[152:155], v[176:179], v[98:101]
	v_mfma_f32_16x16x32_bf16 v[86:89], v[144:147], v[184:187], v[86:89]
	v_mfma_f32_16x16x32_bf16 v[82:85], v[152:155], v[184:187], v[82:85]
	v_mfma_f32_16x16x32_bf16 v[126:129], v[148:151], v[164:167], v[126:129]
	v_mfma_f32_16x16x32_bf16 v[122:125], v[156:159], v[164:167], v[122:125]
	v_mfma_f32_16x16x32_bf16 v[118:121], v[148:151], v[172:175], v[118:121]
	v_mfma_f32_16x16x32_bf16 v[114:117], v[156:159], v[172:175], v[114:117]
	v_mfma_f32_16x16x32_bf16 v[102:105], v[148:151], v[180:183], v[102:105]
	v_mfma_f32_16x16x32_bf16 v[98:101], v[156:159], v[180:183], v[98:101]
	v_mfma_f32_16x16x32_bf16 v[86:89], v[148:151], v[188:191], v[86:89]
	v_mfma_f32_16x16x32_bf16 v[82:85], v[156:159], v[188:191], v[82:85]
	s_barrier
	s_add_i32 s36, 0, 0x14000
	s_add_i32 s0, s33, s40
	v_add_u32_e32 v143, s36, v140
	v_lshl_add_u64 v[192:193], s[24:25], 0, v[194:195]
	s_mov_b32 m0, s0
	ds_read_b128 v[198:201], v143
	ds_read_b128 v[202:205], v143 offset:1024
	ds_read_b128 v[206:209], v143 offset:2048
	ds_read_b128 v[210:213], v143 offset:3072
	global_load_lds_dwordx4 v[192:193], off
	v_lshl_add_u64 v[214:215], s[24:25], 0, v[134:135]
	s_add_i32 m0, s0, 0x2000
	s_nop 0
	global_load_lds_dwordx4 v[214:215], off
	s_barrier
	s_waitcnt lgkmcnt(0)
	v_mfma_f32_16x16x32_bf16 v[110:113], v[198:201], v[160:163], v[110:113]
	v_mfma_f32_16x16x32_bf16 v[106:109], v[206:209], v[160:163], v[106:109]
	v_mfma_f32_16x16x32_bf16 v[94:97], v[198:201], v[168:171], v[94:97]
	v_mfma_f32_16x16x32_bf16 v[90:93], v[206:209], v[168:171], v[90:93]
	v_mfma_f32_16x16x32_bf16 v[78:81], v[198:201], v[176:179], v[78:81]
	v_mfma_f32_16x16x32_bf16 v[74:77], v[206:209], v[176:179], v[74:77]
	v_mfma_f32_16x16x32_bf16 v[70:73], v[198:201], v[184:187], v[70:73]
	v_mfma_f32_16x16x32_bf16 v[66:69], v[206:209], v[184:187], v[66:69]
	v_mfma_f32_16x16x32_bf16 v[110:113], v[202:205], v[164:167], v[110:113]
	v_mfma_f32_16x16x32_bf16 v[106:109], v[210:213], v[164:167], v[106:109]
	v_mfma_f32_16x16x32_bf16 v[94:97], v[202:205], v[172:175], v[94:97]
	v_mfma_f32_16x16x32_bf16 v[90:93], v[210:213], v[172:175], v[90:93]
	v_mfma_f32_16x16x32_bf16 v[78:81], v[202:205], v[180:183], v[78:81]
	v_mfma_f32_16x16x32_bf16 v[74:77], v[210:213], v[180:183], v[74:77]
	v_mfma_f32_16x16x32_bf16 v[70:73], v[202:205], v[188:191], v[70:73]
	v_mfma_f32_16x16x32_bf16 v[66:69], v[210:213], v[188:191], v[66:69]
	s_mov_b32 m0, s9
	v_lshl_add_u64 v[216:217], s[26:27], 0, v[130:131]
	s_barrier
	ds_read_b128 v[160:163], v142 offset:16384
	ds_read_b128 v[164:167], v142 offset:17408
	ds_read_b128 v[168:171], v142 offset:18432
	ds_read_b128 v[172:175], v142 offset:19456
	ds_read_b128 v[176:179], v142 offset:20480
	ds_read_b128 v[180:183], v142 offset:21504
	ds_read_b128 v[184:187], v142 offset:22528
	ds_read_b128 v[188:191], v142 offset:23552
	global_load_lds_dwordx4 v[216:217], off
	v_lshl_add_u64 v[218:219], s[26:27], 0, v[132:133]
	s_mov_b32 m0, s43
	s_nop 0
	global_load_lds_dwordx4 v[218:219], off
	s_waitcnt vmcnt(10)
	s_barrier
	s_waitcnt lgkmcnt(0)
	v_mfma_f32_16x16x32_bf16 v[62:65], v[144:147], v[160:163], v[62:65]
	v_mfma_f32_16x16x32_bf16 v[58:61], v[152:155], v[160:163], v[58:61]
	v_mfma_f32_16x16x32_bf16 v[54:57], v[144:147], v[168:171], v[54:57]
	v_mfma_f32_16x16x32_bf16 v[50:53], v[152:155], v[168:171], v[50:53]
	v_mfma_f32_16x16x32_bf16 v[38:41], v[144:147], v[176:179], v[38:41]
	v_mfma_f32_16x16x32_bf16 v[34:37], v[152:155], v[176:179], v[34:37]
	v_mfma_f32_16x16x32_bf16 v[22:25], v[144:147], v[184:187], v[22:25]
	v_mfma_f32_16x16x32_bf16 v[18:21], v[152:155], v[184:187], v[18:21]
	v_mfma_f32_16x16x32_bf16 v[62:65], v[148:151], v[164:167], v[62:65]
	v_mfma_f32_16x16x32_bf16 v[58:61], v[156:159], v[164:167], v[58:61]
	v_mfma_f32_16x16x32_bf16 v[54:57], v[148:151], v[172:175], v[54:57]
	v_mfma_f32_16x16x32_bf16 v[50:53], v[156:159], v[172:175], v[50:53]
	v_mfma_f32_16x16x32_bf16 v[38:41], v[148:151], v[180:183], v[38:41]
	v_mfma_f32_16x16x32_bf16 v[34:37], v[156:159], v[180:183], v[34:37]
	v_mfma_f32_16x16x32_bf16 v[22:25], v[148:151], v[188:191], v[22:25]
	v_mfma_f32_16x16x32_bf16 v[18:21], v[156:159], v[188:191], v[18:21]
	s_barrier
	s_add_u32 s0, s24, 0x20000
	s_addc_u32 s1, s25, 0
	s_add_i32 s33, s36, s40
	s_mov_b32 m0, s33
	s_nop 0
	global_load_lds_dwordx4 v194, s[0:1]
	s_add_i32 m0, s33, 0x2000
	s_nop 0
	global_load_lds_dwordx4 v134, s[0:1]
	v_add_u32_e32 v156, 0x18000, v140
	ds_read_b128 v[144:147], v156
	ds_read_b128 v[148:151], v156 offset:1024
	ds_read_b128 v[152:155], v156 offset:2048
	ds_read_b128 v[156:159], v156 offset:3072
	s_waitcnt vmcnt(6)
	s_barrier
	v_mfma_f32_16x16x32_bf16 v[46:49], v[198:201], v[160:163], v[46:49]
	v_mfma_f32_16x16x32_bf16 v[42:45], v[206:209], v[160:163], v[42:45]
	v_mfma_f32_16x16x32_bf16 v[30:33], v[198:201], v[168:171], v[30:33]
	v_mfma_f32_16x16x32_bf16 v[26:29], v[206:209], v[168:171], v[26:29]
	v_mfma_f32_16x16x32_bf16 v[14:17], v[198:201], v[176:179], v[14:17]
	v_mfma_f32_16x16x32_bf16 v[10:13], v[206:209], v[176:179], v[10:13]
	v_mfma_f32_16x16x32_bf16 v[6:9], v[198:201], v[184:187], v[6:9]
	v_mfma_f32_16x16x32_bf16 v[2:5], v[206:209], v[184:187], v[2:5]
	v_mfma_f32_16x16x32_bf16 v[46:49], v[202:205], v[164:167], v[46:49]
	v_mfma_f32_16x16x32_bf16 v[42:45], v[210:213], v[164:167], v[42:45]
	v_mfma_f32_16x16x32_bf16 v[30:33], v[202:205], v[172:175], v[30:33]
	v_mfma_f32_16x16x32_bf16 v[26:29], v[210:213], v[172:175], v[26:29]
	v_mfma_f32_16x16x32_bf16 v[14:17], v[202:205], v[180:183], v[14:17]
	v_mfma_f32_16x16x32_bf16 v[10:13], v[210:213], v[180:183], v[10:13]
	v_mfma_f32_16x16x32_bf16 v[6:9], v[202:205], v[188:191], v[6:9]
	v_mfma_f32_16x16x32_bf16 v[2:5], v[210:213], v[188:191], v[2:5]
	s_add_i32 s33, 0, 0x18000
	s_barrier
	s_add_u32 s0, s26, 0x20000
	s_addc_u32 s1, s27, 0
	s_mov_b32 m0, s64
	ds_read_b128 v[160:163], v142 offset:32768
	ds_read_b128 v[164:167], v142 offset:33792
	ds_read_b128 v[168:171], v142 offset:34816
	ds_read_b128 v[172:175], v142 offset:35840
	ds_read_b128 v[176:179], v142 offset:36864
	ds_read_b128 v[180:183], v142 offset:37888
	ds_read_b128 v[184:187], v142 offset:38912
	ds_read_b128 v[188:191], v142 offset:39936
	global_load_lds_dwordx4 v130, s[0:1]
	s_mov_b32 m0, s65
	s_nop 0
	global_load_lds_dwordx4 v132, s[0:1]
	s_waitcnt lgkmcnt(8)
	s_barrier
	s_waitcnt lgkmcnt(0)
	v_mfma_f32_16x16x32_bf16 v[126:129], v[144:147], v[160:163], v[126:129]
	v_mfma_f32_16x16x32_bf16 v[122:125], v[152:155], v[160:163], v[122:125]
	v_mfma_f32_16x16x32_bf16 v[118:121], v[144:147], v[168:171], v[118:121]
	v_mfma_f32_16x16x32_bf16 v[114:117], v[152:155], v[168:171], v[114:117]
	v_mfma_f32_16x16x32_bf16 v[102:105], v[144:147], v[176:179], v[102:105]
	v_mfma_f32_16x16x32_bf16 v[98:101], v[152:155], v[176:179], v[98:101]
	v_mfma_f32_16x16x32_bf16 v[86:89], v[144:147], v[184:187], v[86:89]
	v_mfma_f32_16x16x32_bf16 v[82:85], v[152:155], v[184:187], v[82:85]
	v_mfma_f32_16x16x32_bf16 v[126:129], v[148:151], v[164:167], v[126:129]
	v_mfma_f32_16x16x32_bf16 v[122:125], v[156:159], v[164:167], v[122:125]
	v_mfma_f32_16x16x32_bf16 v[118:121], v[148:151], v[172:175], v[118:121]
	v_mfma_f32_16x16x32_bf16 v[114:117], v[156:159], v[172:175], v[114:117]
	v_mfma_f32_16x16x32_bf16 v[102:105], v[148:151], v[180:183], v[102:105]
	v_mfma_f32_16x16x32_bf16 v[98:101], v[156:159], v[180:183], v[98:101]
	v_mfma_f32_16x16x32_bf16 v[86:89], v[148:151], v[188:191], v[86:89]
	v_mfma_f32_16x16x32_bf16 v[82:85], v[156:159], v[188:191], v[82:85]
	s_barrier
	s_add_i32 s26, 0, 0x1c000
	s_add_i32 s0, s33, s40
	v_add_u32_e32 v143, s26, v140
	v_lshl_add_u64 v[192:193], v[192:193], 0, s[54:55]
	s_mov_b32 m0, s0
	ds_read_b128 v[198:201], v143
	ds_read_b128 v[202:205], v143 offset:1024
	ds_read_b128 v[206:209], v143 offset:2048
	ds_read_b128 v[210:213], v143 offset:3072
	global_load_lds_dwordx4 v[192:193], off
	v_lshl_add_u64 v[192:193], v[214:215], 0, s[54:55]
	s_add_i32 m0, s0, 0x2000
	s_nop 0
	global_load_lds_dwordx4 v[192:193], off
	s_barrier
	s_waitcnt lgkmcnt(0)
	v_mfma_f32_16x16x32_bf16 v[110:113], v[198:201], v[160:163], v[110:113]
	v_mfma_f32_16x16x32_bf16 v[106:109], v[206:209], v[160:163], v[106:109]
	v_mfma_f32_16x16x32_bf16 v[94:97], v[198:201], v[168:171], v[94:97]
	v_mfma_f32_16x16x32_bf16 v[90:93], v[206:209], v[168:171], v[90:93]
	v_mfma_f32_16x16x32_bf16 v[78:81], v[198:201], v[176:179], v[78:81]
	v_mfma_f32_16x16x32_bf16 v[74:77], v[206:209], v[176:179], v[74:77]
	v_mfma_f32_16x16x32_bf16 v[70:73], v[198:201], v[184:187], v[70:73]
	v_mfma_f32_16x16x32_bf16 v[66:69], v[206:209], v[184:187], v[66:69]
	v_mfma_f32_16x16x32_bf16 v[110:113], v[202:205], v[164:167], v[110:113]
	v_mfma_f32_16x16x32_bf16 v[106:109], v[210:213], v[164:167], v[106:109]
	v_mfma_f32_16x16x32_bf16 v[94:97], v[202:205], v[172:175], v[94:97]
	v_mfma_f32_16x16x32_bf16 v[90:93], v[210:213], v[172:175], v[90:93]
	v_mfma_f32_16x16x32_bf16 v[78:81], v[202:205], v[180:183], v[78:81]
	v_mfma_f32_16x16x32_bf16 v[74:77], v[210:213], v[180:183], v[74:77]
	v_mfma_f32_16x16x32_bf16 v[70:73], v[202:205], v[188:191], v[70:73]
	v_mfma_f32_16x16x32_bf16 v[66:69], v[210:213], v[188:191], v[66:69]
	s_mov_b32 m0, s66
	v_lshl_add_u64 v[192:193], v[216:217], 0, s[54:55]
	s_barrier
	ds_read_b128 v[160:163], v142 offset:49152
	ds_read_b128 v[164:167], v142 offset:50176
	ds_read_b128 v[168:171], v142 offset:51200
	ds_read_b128 v[172:175], v142 offset:52224
	ds_read_b128 v[176:179], v142 offset:53248
	ds_read_b128 v[180:183], v142 offset:54272
	ds_read_b128 v[184:187], v142 offset:55296
	ds_read_b128 v[188:191], v142 offset:56320
	global_load_lds_dwordx4 v[192:193], off
	v_lshl_add_u64 v[192:193], v[218:219], 0, s[54:55]
	s_mov_b32 m0, s67
	s_nop 0
	global_load_lds_dwordx4 v[192:193], off
	s_waitcnt vmcnt(10)
	s_barrier
	s_waitcnt lgkmcnt(0)
	v_mfma_f32_16x16x32_bf16 v[62:65], v[144:147], v[160:163], v[62:65]
	v_mfma_f32_16x16x32_bf16 v[58:61], v[152:155], v[160:163], v[58:61]
	v_mfma_f32_16x16x32_bf16 v[54:57], v[144:147], v[168:171], v[54:57]
	v_mfma_f32_16x16x32_bf16 v[50:53], v[152:155], v[168:171], v[50:53]
	v_mfma_f32_16x16x32_bf16 v[38:41], v[144:147], v[176:179], v[38:41]
	v_mfma_f32_16x16x32_bf16 v[34:37], v[152:155], v[176:179], v[34:37]
	v_mfma_f32_16x16x32_bf16 v[22:25], v[144:147], v[184:187], v[22:25]
	v_mfma_f32_16x16x32_bf16 v[18:21], v[152:155], v[184:187], v[18:21]
	v_mfma_f32_16x16x32_bf16 v[62:65], v[148:151], v[164:167], v[62:65]
	v_mfma_f32_16x16x32_bf16 v[58:61], v[156:159], v[164:167], v[58:61]
	v_mfma_f32_16x16x32_bf16 v[54:57], v[148:151], v[172:175], v[54:57]
	v_mfma_f32_16x16x32_bf16 v[50:53], v[156:159], v[172:175], v[50:53]
	v_mfma_f32_16x16x32_bf16 v[38:41], v[148:151], v[180:183], v[38:41]
	v_mfma_f32_16x16x32_bf16 v[34:37], v[156:159], v[180:183], v[34:37]
	v_mfma_f32_16x16x32_bf16 v[22:25], v[148:151], v[188:191], v[22:25]
	v_mfma_f32_16x16x32_bf16 v[18:21], v[156:159], v[188:191], v[18:21]
	s_barrier
	s_add_u32 s0, s24, 0x20080
	s_addc_u32 s1, s25, 0
	s_add_i32 s24, s26, s40
	s_mov_b32 m0, s24
	s_nop 0
	global_load_lds_dwordx4 v194, s[0:1]
	s_add_i32 m0, s24, 0x2000
	s_nop 0
	global_load_lds_dwordx4 v134, s[0:1]
	v_add_u32_e32 v156, 0x10000, v140
	ds_read_b128 v[144:147], v156
	ds_read_b128 v[148:151], v156 offset:1024
	ds_read_b128 v[152:155], v156 offset:2048
	ds_read_b128 v[156:159], v156 offset:3072
	s_waitcnt vmcnt(6)
	s_barrier
	v_mfma_f32_16x16x32_bf16 v[46:49], v[198:201], v[160:163], v[46:49]
	v_mfma_f32_16x16x32_bf16 v[42:45], v[206:209], v[160:163], v[42:45]
	v_mfma_f32_16x16x32_bf16 v[30:33], v[198:201], v[168:171], v[30:33]
	v_mfma_f32_16x16x32_bf16 v[26:29], v[206:209], v[168:171], v[26:29]
	v_mfma_f32_16x16x32_bf16 v[14:17], v[198:201], v[176:179], v[14:17]
	v_mfma_f32_16x16x32_bf16 v[10:13], v[206:209], v[176:179], v[10:13]
	v_mfma_f32_16x16x32_bf16 v[6:9], v[198:201], v[184:187], v[6:9]
	v_mfma_f32_16x16x32_bf16 v[2:5], v[206:209], v[184:187], v[2:5]
	v_mfma_f32_16x16x32_bf16 v[46:49], v[202:205], v[164:167], v[46:49]
	v_mfma_f32_16x16x32_bf16 v[42:45], v[210:213], v[164:167], v[42:45]
	v_mfma_f32_16x16x32_bf16 v[30:33], v[202:205], v[172:175], v[30:33]
	v_mfma_f32_16x16x32_bf16 v[26:29], v[210:213], v[172:175], v[26:29]
	v_mfma_f32_16x16x32_bf16 v[14:17], v[202:205], v[180:183], v[14:17]
	v_mfma_f32_16x16x32_bf16 v[10:13], v[210:213], v[180:183], v[10:13]
	v_mfma_f32_16x16x32_bf16 v[6:9], v[202:205], v[188:191], v[6:9]
	v_mfma_f32_16x16x32_bf16 v[2:5], v[210:213], v[188:191], v[2:5]
	s_add_i32 s77, s77, 2
	s_add_u32 s22, s22, 0x100
	s_addc_u32 s23, s23, 0
	s_add_u32 s75, s75, 0x100
	s_addc_u32 s76, s76, 0
	s_cmp_gt_u32 s77, 5
	s_barrier
	s_cbranch_scc0 .LBB0_2563
	s_waitcnt lgkmcnt(0)
	v_lshl_add_u32 v144, s8, 8, v1
	v_lshl_or_b32 v146, s68, 8, v141
	v_ashrrev_i32_e32 v145, 31, v144
	v_lshlrev_b64 v[148:149], 11, v[144:145]
	v_ashrrev_i32_e32 v147, 31, v146
	v_lshl_add_u64 v[148:149], s[6:7], 0, v[148:149]
	v_cvt_pk_bf16_f32 v126, v126, v127
	v_cvt_pk_bf16_f32 v127, v128, v129
	v_cvt_pk_bf16_f32 v128, v122, v123
	v_lshlrev_b64 v[122:123], 1, v[146:147]
	v_cvt_pk_bf16_f32 v129, v124, v125
	v_lshl_add_u64 v[124:125], v[148:149], 0, v[122:123]
	s_mov_b64 s[0:1], 0x40000
	v_cvt_pk_bf16_f32 v62, v62, v63
	v_cvt_pk_bf16_f32 v63, v64, v65
	v_cvt_pk_bf16_f32 v64, v58, v59
	v_lshl_add_u64 v[58:59], v[124:125], 0, s[0:1]
	s_mov_b32 s0, 0x40000
	v_cvt_pk_bf16_f32 v110, v110, v111
	v_cvt_pk_bf16_f32 v111, v112, v113
	v_cvt_pk_bf16_f32 v112, v106, v107
	v_or_b32_e32 v106, 16, v144
	v_cvt_pk_bf16_f32 v65, v60, v61
	v_add_co_u32_e32 v60, vcc, s0, v124
	v_cvt_pk_bf16_f32 v46, v46, v47
	v_cvt_pk_bf16_f32 v47, v48, v49
	v_cvt_pk_bf16_f32 v48, v42, v43
	v_cvt_pk_bf16_f32 v49, v44, v45
	s_mov_b64 s[0:1], 0x48000
	v_ashrrev_i32_e32 v107, 31, v106
	v_addc_co_u32_e32 v61, vcc, 0, v125, vcc
	global_store_dwordx4 v[58:59], v[46:49], off offset:256
	v_cvt_pk_bf16_f32 v113, v108, v109
	v_lshlrev_b64 v[106:107], 11, v[106:107]
	v_lshl_add_u64 v[46:47], v[124:125], 0, s[0:1]
	s_mov_b32 s0, 0x48000
	v_cvt_pk_bf16_f32 v94, v94, v95
	v_cvt_pk_bf16_f32 v95, v96, v97
	v_cvt_pk_bf16_f32 v96, v90, v91
	v_or_b32_e32 v90, 32, v144
	v_add_co_u32_e32 v48, vcc, s0, v124
	v_cvt_pk_bf16_f32 v30, v30, v31
	v_cvt_pk_bf16_f32 v31, v32, v33
	v_cvt_pk_bf16_f32 v32, v26, v27
	v_cvt_pk_bf16_f32 v33, v28, v29
	s_mov_b64 s[0:1], 0x50000
	global_store_dwordx4 v[124:125], v[110:113], off offset:256
	v_ashrrev_i32_e32 v91, 31, v90
	v_addc_co_u32_e32 v49, vcc, 0, v125, vcc
	v_lshl_add_u64 v[110:111], s[6:7], 0, v[106:107]
	global_store_dwordx4 v[46:47], v[30:33], off offset:256
	v_lshl_add_u64 v[110:111], v[110:111], 0, v[122:123]
	v_cvt_pk_bf16_f32 v97, v92, v93
	v_lshl_add_u64 v[30:31], v[124:125], 0, s[0:1]
	s_mov_b32 s0, 0x50000
	v_lshlrev_b64 v[90:91], 11, v[90:91]
	v_cvt_pk_bf16_f32 v78, v78, v79
	v_cvt_pk_bf16_f32 v79, v80, v81
	v_cvt_pk_bf16_f32 v80, v74, v75
	v_or_b32_e32 v74, 48, v144
	v_add_co_u32_e32 v32, vcc, s0, v124
	v_cvt_pk_bf16_f32 v14, v14, v15
	v_cvt_pk_bf16_f32 v15, v16, v17
	v_cvt_pk_bf16_f32 v16, v10, v11
	v_cvt_pk_bf16_f32 v17, v12, v13
	s_mov_b64 s[0:1], 0x58000
	global_store_dwordx4 v[110:111], v[94:97], off offset:256
	v_ashrrev_i32_e32 v75, 31, v74
	v_addc_co_u32_e32 v33, vcc, 0, v125, vcc
	v_lshl_add_u64 v[94:95], s[6:7], 0, v[90:91]
	global_store_dwordx4 v[30:31], v[14:17], off offset:256
	v_lshl_add_u64 v[94:95], v[94:95], 0, v[122:123]
	v_cvt_pk_bf16_f32 v81, v76, v77
	v_lshl_add_u64 v[14:15], v[124:125], 0, s[0:1]
	s_mov_b32 s0, 0x58000
	v_lshlrev_b64 v[74:75], 11, v[74:75]
	v_add_co_u32_e32 v16, vcc, s0, v124
	global_store_dwordx4 v[94:95], v[78:81], off offset:256
	s_nop 0
	v_addc_co_u32_e32 v17, vcc, 0, v125, vcc
	v_lshl_add_u64 v[78:79], s[6:7], 0, v[74:75]
	v_cvt_pk_bf16_f32 v106, v118, v119
	v_cvt_pk_bf16_f32 v107, v120, v121
	v_cvt_pk_bf16_f32 v108, v114, v115
	v_cvt_pk_bf16_f32 v109, v116, v117
	v_cvt_pk_bf16_f32 v90, v102, v103
	v_cvt_pk_bf16_f32 v91, v104, v105
	v_cvt_pk_bf16_f32 v92, v98, v99
	v_cvt_pk_bf16_f32 v93, v100, v101
	v_cvt_pk_bf16_f32 v74, v86, v87
	v_cvt_pk_bf16_f32 v75, v88, v89
	v_cvt_pk_bf16_f32 v76, v82, v83
	v_cvt_pk_bf16_f32 v77, v84, v85
	v_lshl_add_u64 v[78:79], v[78:79], 0, v[122:123]
	v_cvt_pk_bf16_f32 v70, v70, v71
	v_cvt_pk_bf16_f32 v71, v72, v73
	v_cvt_pk_bf16_f32 v72, v66, v67
	v_cvt_pk_bf16_f32 v73, v68, v69
	v_cvt_pk_bf16_f32 v42, v54, v55
	v_cvt_pk_bf16_f32 v43, v56, v57
	v_cvt_pk_bf16_f32 v44, v50, v51
	v_cvt_pk_bf16_f32 v45, v52, v53
	v_cvt_pk_bf16_f32 v26, v38, v39
	v_cvt_pk_bf16_f32 v27, v40, v41
	v_cvt_pk_bf16_f32 v28, v34, v35
	v_cvt_pk_bf16_f32 v29, v36, v37
	v_cvt_pk_bf16_f32 v10, v22, v23
	v_cvt_pk_bf16_f32 v11, v24, v25
	v_cvt_pk_bf16_f32 v12, v18, v19
	v_cvt_pk_bf16_f32 v13, v20, v21
	v_cvt_pk_bf16_f32 v6, v6, v7
	v_cvt_pk_bf16_f32 v7, v8, v9
	v_cvt_pk_bf16_f32 v8, v2, v3
	v_cvt_pk_bf16_f32 v9, v4, v5
	s_and_b64 vcc, exec, s[18:19]
	s_mov_b32 s68, s14
	s_mov_b32 s8, s10
	s_mov_b64 s[24:25], s[20:21]
	s_mov_b64 s[22:23], s[16:17]
	global_store_dwordx4 v[124:125], v[126:129], off
	global_store_dwordx4 v[110:111], v[106:109], off
	global_store_dwordx4 v[94:95], v[90:93], off
	global_store_dwordx4 v[78:79], v[74:77], off
	global_store_dwordx4 v[78:79], v[70:73], off offset:256
	global_store_dwordx4 v[60:61], v[62:65], off
	global_store_dwordx4 v[48:49], v[42:45], off
	global_store_dwordx4 v[32:33], v[26:29], off
	global_store_dwordx4 v[16:17], v[10:13], off
	global_store_dwordx4 v[14:15], v[6:9], off offset:256
	s_cbranch_vccz .LBB0_2555
	s_waitcnt vmcnt(0)
	s_cmpk_gt_u32 s29, 0xff
	s_cbranch_scc1 .LBB0_2567
	s_barrier
